# HGRN: QT stored in MFMA-fragment-major order so the state recurrence loads each Q fragment with one coalesced dwordx4 (was two scattered dwordx2)
# speedup vs baseline: 1.0261x; 1.0192x over previous
; #define LAS __attribute__((address_space(3)))
; __device__ __forceinline__ void hgrn_x1_unit(const Args& a, int layer, int unit, LAS unsigned char* lds) {
;     int tid = threadIdx.x; asm volatile("" : "+v"(tid)); const int lane = tid & 63; const int wave = __builtin_amdgcn_readfirstlane(tid >> 6);
;     size_t wz_ = 0; asm volatile("" : "+s"(wz_)); unsigned char* ws = a.ws + wz_;
;     const int blk = unit & 63, h = (unit >> 6) & 7, b = unit >> 9;
;     const bf16* PROJ = (const bf16*)(ws + WS_PROJ);
;     bf16* QT = (bf16*)(ws + WS_HQT); bf16* KT = (bf16*)(ws + WS_HKT) + (size_t)unit * 4096; bf16* VT = (bf16*)(ws + WS_HVT) + (size_t)unit * 4096;
;     float* DEC = (float*)(ws + WS_HDEC) + (size_t)unit * 128; float* OI = (float*)(ws + WS_HOI);
;     LAS float* TOT = (LAS float*)(lds + HX_TOT);
;     const size_t tok0 = (size_t)b * SEQ + blk * HB;
;     const int d = tid & 127, tq = tid >> 7;
;     const float lb = ((const float*)(ws + WS_LB))[layer * 1024 + h * 128 + d];
;     float q[8], kk[8], c[8]; unsigned short vv[8];
;     float run = 0.f;
; #pragma unroll
;     for (int i = 0; i < 8; ++i) {
;         const bf16* pr = PROJ + (tok0 + 8 * tq + i) * DIN + h * 128 + d;
;         q[i] = bf2f(pr[C_QA]); vv[i] = pr[C_IA];
;         float z = bf2f(pr[C_FA]); z = fminf(fmaxf(z, -30.f), 30.f);
;         const float e = __expf(-z), sp = 1.0f / (1.0f + e), sn = e / (1.0f + e);
;         const float f = lb + (1.0f - lb) * sp; kk[i] = (1.0f - lb) * sn;
;         run += __logf(f); c[i] = run;
; template <int LAYER>
; __device__ __forceinline__ void layer_phases(const Args& args, LAS unsigned char* lds, const XcdBarrier& bar, int lo, int hi) {
;     ...
;         for (;;) {
;             __syncthreads();
;             if (threadIdx.x == 0) *slot = (int)__hip_atomic_fetch_add(ctr, 1u, __ATOMIC_RELAXED, __HIP_MEMORY_SCOPE_AGENT);
;             __syncthreads();
;             const int it = __builtin_amdgcn_readfirstlane(*slot);
;             if (it >= 256 + 1024 + 2048) break;
;             if (it < 256) s5_unit(args, LAYER, it, lds);
;             else if (it < 1280) { const int j = it - 256, n = 31 - (j >> 5), b = (j >> 3) & 3, hp = j & 7, n0_ = (b & 1) ? 31 - n : n; attn_item(args, LAYER, b * 256 + n0_ * 8 + hp, lds); }
;             else hgrn_x1_unit(args, LAYER, it - 1280, lds);
.LBB0_321:
	s_or_b64 exec, exec, s[4:5]
	s_waitcnt lgkmcnt(0)
	s_barrier
	ds_read_b32 v2, v1
	s_mov_b64 s[4:5], -1
	s_waitcnt lgkmcnt(0)
	v_readfirstlane_b32 s85, v2
	s_cmpk_gt_i32 s85, 0xcff
	s_cbranch_scc1 .LBB0_316
	s_cmpk_gt_i32 s85, 0xff
	s_cbranch_scc0 .LBB0_349
	s_cmpk_gt_u32 s85, 0x4ff
	s_cbranch_scc0 .LBB0_327
	s_add_i32 s22, s85, 0xfffffb00
	v_mov_b32_e32 v14, v0
	s_mov_b64 s[4:5], 0
	s_add_u32 s8, s20, s4
	s_addc_u32 s9, s21, s5
	s_lshl_b32 s4, s22, 2
	s_lshl_b32 s5, s22, 5
	s_and_b32 s4, s4, 0x1800
	s_and_b32 s5, s5, 0x7e0
	s_or_b32 s10, s4, s5
	s_lshl_b32 s4, s22, 1
	v_and_b32_e32 v15, 0x7f, v14
	s_and_b32 s12, s4, 0x380
	v_or_b32_e32 v2, s12, v15
	v_lshlrev_b32_e32 v82, 2, v2
	v_lshl_add_u64 v[2:3], s[8:9], 0, v[82:83]
	s_mov_b32 s4, 0x21480000
	v_add_co_u32_e32 v10, vcc, s4, v2
	s_lshl_b32 s4, s12, 1
	v_ashrrev_i32_e32 v16, 7, v14
	s_add_u32 s4, s8, s4
	v_lshlrev_b32_e32 v2, 3, v16
	v_lshlrev_b32_e32 v82, 1, v15
	s_addc_u32 s5, s9, 0
	s_mov_b32 s11, s23
	v_addc_co_u32_e32 v11, vcc, 0, v3, vcc
	v_ashrrev_i32_e32 v3, 31, v2
	v_lshl_add_u64 v[6:7], s[4:5], 0, v[82:83]
	s_mov_b64 s[4:5], 0x2d482000
	v_lshl_add_u64 v[4:5], v[2:3], 0, s[10:11]
	v_lshl_add_u64 v[8:9], v[6:7], 0, s[4:5]
	v_mad_i64_i32 v[8:9], s[4:5], v4, s72, v[8:9]
	s_movk_i32 s5, 0x6000
	s_nop 0
	v_add_co_u32_e32 v12, vcc, s5, v8
	s_movk_i32 s4, 0x5000
	s_nop 0
	v_addc_co_u32_e32 v13, vcc, 0, v9, vcc
	global_load_dword v23, v[10:11], off
	global_load_ushort v20, v[12:13], off
	global_load_ushort v21, v[8:9], off offset:2048
	v_add_co_u32_e32 v10, vcc, s4, v8
	s_movk_i32 s4, 0x1000
	s_nop 0
	v_addc_co_u32_e32 v11, vcc, 0, v9, vcc
	s_waitcnt vmcnt(18)
	v_add_co_u32_e32 v18, vcc, s4, v8
	s_mov_b32 s4, 0xb000
	s_nop 0
	v_addc_co_u32_e32 v19, vcc, 0, v9, vcc
	global_load_ushort v17, v[12:13], off offset:2048
	s_nop 0
	global_load_ushort v18, v[18:19], off
	s_nop 0
	global_load_ushort v12, v[8:9], off
	global_load_ushort v13, v[10:11], off offset:2048
	v_add_co_u32_e32 v10, vcc, s4, v8
	v_lshlrev_b64 v[4:5], 11, v[4:5]
	s_nop 0
	v_addc_co_u32_e32 v11, vcc, 0, v9, vcc
	global_load_ushort v36, v[10:11], off offset:2048
	v_readfirstlane_b32 s13, v14
	s_waitcnt vmcnt(7)
	v_sub_f32_e32 v24, 1.0, v23
	s_waitcnt vmcnt(6)
	v_lshlrev_b32_e32 v11, 16, v20
	s_waitcnt vmcnt(5)
	v_lshlrev_b32_e32 v10, 16, v21
	v_max_f32_e32 v10, v10, v10
	v_med3_f32 v10, v10, s73, v102
	v_mul_f32_e32 v10, 0xbfb8aa3b, v10
	v_exp_f32_e32 v10, v10
	v_max_f32_e32 v11, v11, v11
	v_med3_f32 v11, v11, s73, v102
	v_mul_f32_e32 v11, 0xbfb8aa3b, v11
	v_exp_f32_e32 v37, v11
	v_add_f32_e32 v11, 1.0, v10
	s_waitcnt vmcnt(2)
	v_lshlrev_b32_e32 v20, 16, v12
	v_div_scale_f32 v12, s[4:5], v11, v11, 1.0
	v_rcp_f32_e32 v26, v12
	v_div_scale_f32 v21, s[4:5], v11, v11, v10
	v_rcp_f32_e32 v27, v21
	v_fma_f32 v30, -v12, v26, 1.0
	s_waitcnt vmcnt(1)
	v_lshlrev_b32_e32 v19, 16, v13
	v_div_scale_f32 v13, vcc, 1.0, v11, 1.0
	v_fmac_f32_e32 v26, v30, v26
	v_mul_f32_e32 v30, v13, v26
	v_fma_f32 v31, -v21, v27, 1.0
	v_fma_f32 v33, -v12, v30, v13
	v_div_scale_f32 v22, s[4:5], v10, v11, v10
	v_fmac_f32_e32 v27, v31, v27
	v_fmac_f32_e32 v30, v33, v26
	v_mul_f32_e32 v31, v22, v27
	v_fma_f32 v12, -v12, v30, v13
	v_fma_f32 v34, -v21, v31, v22
	v_div_fmas_f32 v12, v12, v26, v30
	v_fmac_f32_e32 v31, v34, v27
	v_div_fixup_f32 v12, v12, v11, 1.0
	v_fma_f32 v13, -v21, v31, v22
	s_mov_b64 vcc, s[4:5]
	v_fma_f32 v12, v24, v12, v23
	v_div_fmas_f32 v13, v13, v27, v31
	v_cmp_gt_f32_e32 vcc, s74, v12
	v_add_f32_e32 v38, 1.0, v37
	v_div_scale_f32 v25, s[6:7], v38, v38, 1.0
	v_cndmask_b32_e64 v21, 0, 32, vcc
	v_ldexp_f32 v12, v12, v21
	v_log_f32_e32 v12, v12
	v_rcp_f32_e32 v28, v25
	v_div_fixup_f32 v10, v13, v11, v10
	v_div_scale_f32 v29, s[6:7], 1.0, v38, 1.0
	v_mul_f32_e32 v11, 0x3f317217, v12
	v_fma_f32 v11, v12, s75, -v11
	v_fma_f32 v32, -v25, v28, 1.0
	v_fmac_f32_e32 v11, 0x3377d1cf, v12
	v_fmac_f32_e32 v28, v32, v28
	v_mul_f32_e32 v21, v24, v10
	v_cndmask_b32_e32 v10, 0, v103, vcc
	v_fmac_f32_e32 v11, 0x3f317217, v12
	v_cmp_lt_f32_e64 vcc, |v12|, s76
	v_mul_f32_e32 v32, v29, v28
	v_fma_f32 v35, -v25, v32, v29
	v_cndmask_b32_e32 v11, v12, v11, vcc
	v_div_scale_f32 v12, s[4:5], v38, v38, v37
	v_rcp_f32_e32 v39, v12
	v_fmac_f32_e32 v32, v35, v28
	v_sub_f32_e32 v10, v11, v10
	v_add_f32_e32 v22, 0, v10
	v_fma_f32 v10, -v25, v32, v29
	s_mov_b64 vcc, s[6:7]
	v_div_fmas_f32 v10, v10, v28, v32
	v_div_fixup_f32 v13, v10, v38, 1.0
	v_fma_f32 v10, -v12, v39, 1.0
	v_fmac_f32_e32 v39, v10, v39
	v_div_scale_f32 v25, vcc, v37, v38, v37
	s_mov_b32 s4, 0xc000
	v_mul_f32_e32 v40, v25, v39
	v_add_co_u32_e64 v10, s[4:5], s4, v8
	v_fma_f32 v26, -v12, v40, v25
	s_nop 0
	v_addc_co_u32_e64 v11, s[4:5], 0, v9, s[4:5]
	v_fmac_f32_e32 v40, v26, v39
	s_mov_b32 s4, 0x10000
	v_fma_f32 v42, -v12, v40, v25
	v_add_co_u32_e64 v12, s[4:5], s4, v8
	global_load_ushort v41, v[10:11], off offset:-4096
	v_fma_f32 v43, v24, v13, v23
	v_addc_co_u32_e64 v13, s[4:5], 0, v9, s[4:5]
	v_add_co_u32_e64 v28, s[4:5], s35, v8
	s_mov_b64 s[6:7], 0x45c82000
	s_nop 0
	v_addc_co_u32_e64 v29, s[4:5], 0, v9, s[4:5]
	v_add_co_u32_e64 v26, s[4:5], s16, v8
	v_lshl_add_u64 v[6:7], v[6:7], 0, s[6:7]
	s_nop 0
	v_addc_co_u32_e64 v27, s[4:5], 0, v9, s[4:5]
	s_mov_b32 s4, 0x1b000
	s_nop 0
	v_add_co_u32_e64 v30, s[4:5], s4, v8
	s_movk_i32 s6, 0x880
	s_nop 0
	v_addc_co_u32_e64 v31, s[4:5], 0, v9, s[4:5]
	s_mov_b32 s4, 0x1c000
	s_nop 0
	v_add_co_u32_e64 v32, s[4:5], s4, v8
	s_waitcnt vmcnt(0)
; __device__ __forceinline__ float bf2f(bf16 b) { return __uint_as_float(((unsigned)b) << 16); }
; __device__ __forceinline__ void hgrn_x1_unit(const Args& a, int layer, int unit, LAS unsigned char* lds) {
;     ...
;     for (int i = 0; i < 8; ++i) {
;         const bf16* pr = PROJ + (tok0 + 8 * tq + i) * DIN + h * 128 + d;
;         q[i] = bf2f(pr[C_QA]); vv[i] = pr[C_IA];
;         float z = bf2f(pr[C_FA]); z = fminf(fmaxf(z, -30.f), 30.f);
;         const float e = __expf(-z), sp = 1.0f / (1.0f + e), sn = e / (1.0f + e);
;         const float f = lb + (1.0f - lb) * sp; kk[i] = (1.0f - lb) * sn;
;         run += __logf(f); c[i] = run;
;     }
	v_lshlrev_b32_e32 v54, 16, v41
	v_addc_co_u32_e64 v33, s[4:5], 0, v9, s[4:5]
	s_mov_b32 s4, 0x21000
	s_nop 0
	v_add_co_u32_e64 v34, s[4:5], s4, v8
	s_nop 1
	v_addc_co_u32_e64 v35, s[4:5], 0, v9, s[4:5]
	global_load_ushort v44, v[12:13], off offset:2048
	global_load_ushort v25, v[28:29], off offset:2048
	global_load_ushort v45, v[26:27], off offset:2048
	global_load_ushort v46, v[30:31], off offset:2048
	s_nop 0
	global_load_ushort v26, v[32:33], off offset:2048
	s_nop 0
	global_load_ushort v34, v[34:35], off offset:2048
	s_nop 0
	global_load_ushort v32, v[32:33], off
	s_nop 0
	global_load_ushort v33, v[28:29], off
	v_cmp_gt_f32_e64 s[4:5], s74, v43
	v_div_fmas_f32 v13, v42, v39, v40
	v_div_fixup_f32 v13, v13, v38, v37
	v_cndmask_b32_e64 v12, 0, 32, s[4:5]
	v_ldexp_f32 v12, v43, v12
	v_log_f32_e32 v12, v12
	v_mul_f32_e32 v52, v24, v13
	v_mul_f32_e32 v13, 0x3f317217, v12
	v_fma_f32 v13, v12, s75, -v13
	v_fmac_f32_e32 v13, 0x3377d1cf, v12
	v_fmac_f32_e32 v13, 0x3f317217, v12
	v_cmp_lt_f32_e64 vcc, |v12|, s76
	s_waitcnt vmcnt(7)
	v_lshlrev_b32_e32 v57, 16, v44
	v_cndmask_b32_e32 v12, v12, v13, vcc
	v_lshlrev_b32_e32 v13, 16, v36
	v_max_f32_e32 v13, v13, v13
	v_med3_f32 v13, v13, s73, v102
	v_mul_f32_e32 v13, 0xbfb8aa3b, v13
	v_exp_f32_e32 v35, v13
	v_cndmask_b32_e64 v13, 0, v103, s[4:5]
	v_add_co_u32_e32 v28, vcc, s17, v8
	v_add_f32_e32 v36, 1.0, v35
	v_div_scale_f32 v37, s[4:5], v36, v36, 1.0
	v_sub_f32_e32 v12, v12, v13
	v_addc_co_u32_e32 v29, vcc, 0, v9, vcc
	s_mov_b32 s4, 0x22000
	v_add_f32_e32 v53, v22, v12
	v_add_co_u32_e32 v12, vcc, s4, v8
	s_mov_b32 s4, 0x27000
	s_nop 0
	v_addc_co_u32_e32 v13, vcc, 0, v9, vcc
	v_add_co_u32_e32 v30, vcc, s4, v8
	v_rcp_f32_e32 v38, v37
	s_nop 0
	v_addc_co_u32_e32 v31, vcc, 0, v9, vcc
	global_load_ushort v10, v[10:11], off
	s_nop 0
	global_load_ushort v39, v[28:29], off offset:-4096
	global_load_ushort v11, v[28:29], off
	s_nop 0
	global_load_ushort v28, v[12:13], off offset:-4096
	global_load_ushort v27, v[30:31], off offset:2048
	v_fma_f32 v29, -v37, v38, 1.0
	v_fmac_f32_e32 v38, v29, v38
	v_div_scale_f32 v29, vcc, 1.0, v36, 1.0
	v_mul_f32_e32 v40, v29, v38
	v_fma_f32 v41, -v37, v40, v29
	v_fmac_f32_e32 v40, v41, v38
	v_fma_f32 v29, -v37, v40, v29
	v_div_scale_f32 v37, s[4:5], v36, v36, v35
	v_rcp_f32_e32 v41, v37
	v_div_fmas_f32 v29, v29, v38, v40
	v_div_fixup_f32 v29, v29, v36, 1.0
	v_fma_f32 v29, v24, v29, v23
	v_fma_f32 v38, -v37, v41, 1.0
	v_fmac_f32_e32 v41, v38, v41
	v_div_scale_f32 v38, vcc, v35, v36, v35
	v_mul_f32_e32 v40, v38, v41
	v_fma_f32 v42, -v37, v40, v38
	v_fmac_f32_e32 v40, v42, v41
	v_cmp_gt_f32_e64 s[4:5], s74, v29
	v_fma_f32 v37, -v37, v40, v38
	s_waitcnt vmcnt(5)
	v_lshlrev_b32_e32 v33, 16, v33
	v_cndmask_b32_e64 v38, 0, 32, s[4:5]
	v_ldexp_f32 v29, v29, v38
	v_log_f32_e32 v29, v29
	v_max_f32_e32 v33, v33, v33
	v_med3_f32 v33, v33, s73, v102
	v_div_fmas_f32 v37, v37, v41, v40
	v_mul_f32_e32 v33, 0xbfb8aa3b, v33
	v_div_fixup_f32 v35, v37, v36, v35
	v_exp_f32_e32 v33, v33
	v_mul_f32_e32 v55, v24, v35
	v_mul_f32_e32 v35, 0x3f317217, v29
	v_fma_f32 v35, v29, s75, -v35
	v_fmac_f32_e32 v35, 0x3377d1cf, v29
	v_fmac_f32_e32 v35, 0x3f317217, v29
	v_cmp_lt_f32_e64 vcc, |v29|, s76
	v_add_f32_e32 v36, 1.0, v33
	v_lshlrev_b32_e32 v32, 16, v32
	v_cndmask_b32_e32 v29, v29, v35, vcc
	v_cndmask_b32_e64 v35, 0, v103, s[4:5]
	v_div_scale_f32 v37, s[4:5], v36, v36, 1.0
	v_rcp_f32_e32 v38, v37
	v_sub_f32_e32 v29, v29, v35
	v_add_f32_e32 v56, v53, v29
	v_max_f32_e32 v32, v32, v32
	v_fma_f32 v29, -v37, v38, 1.0
	v_fmac_f32_e32 v38, v29, v38
	v_div_scale_f32 v29, vcc, 1.0, v36, 1.0
	v_mul_f32_e32 v35, v29, v38
	v_fma_f32 v40, -v37, v35, v29
	v_fmac_f32_e32 v35, v40, v38
	v_fma_f32 v29, -v37, v35, v29
	v_div_scale_f32 v37, s[4:5], v36, v36, v33
	v_rcp_f32_e32 v40, v37
	v_div_fmas_f32 v29, v29, v38, v35
	v_div_fixup_f32 v29, v29, v36, 1.0
	v_fma_f32 v29, v24, v29, v23
	v_fma_f32 v35, -v37, v40, 1.0
	v_fmac_f32_e32 v40, v35, v40
	v_div_scale_f32 v35, vcc, v33, v36, v33
	v_mul_f32_e32 v38, v35, v40
	v_fma_f32 v41, -v37, v38, v35
	v_fmac_f32_e32 v38, v41, v40
	v_fma_f32 v35, -v37, v38, v35
	v_cmp_gt_f32_e64 s[4:5], s74, v29
	v_div_fmas_f32 v35, v35, v40, v38
	v_div_fixup_f32 v33, v35, v36, v33
	v_cndmask_b32_e64 v37, 0, 32, s[4:5]
	v_ldexp_f32 v29, v29, v37
	v_lshlrev_b32_e32 v35, 16, v45
	v_log_f32_e32 v29, v29
	v_max_f32_e32 v35, v35, v35
	v_med3_f32 v35, v35, s73, v102
	v_mul_f32_e32 v35, 0xbfb8aa3b, v35
	v_exp_f32_e32 v35, v35
	v_mul_f32_e32 v58, v24, v33
	v_mul_f32_e32 v33, 0x3f317217, v29
	v_fma_f32 v33, v29, s75, -v33
	v_fmac_f32_e32 v33, 0x3377d1cf, v29
	v_fmac_f32_e32 v33, 0x3f317217, v29
	v_cmp_lt_f32_e64 vcc, |v29|, s76
	v_add_f32_e32 v36, 1.0, v35
	s_waitcnt vmcnt(3)
	v_lshlrev_b32_e32 v60, 16, v39
	v_cndmask_b32_e32 v29, v29, v33, vcc
	v_cndmask_b32_e64 v33, 0, v103, s[4:5]
	v_div_scale_f32 v37, s[4:5], v36, v36, 1.0
	v_rcp_f32_e32 v38, v37
	v_sub_f32_e32 v29, v29, v33
	v_add_f32_e32 v59, v56, v29
	v_med3_f32 v32, v32, s73, v102
	v_fma_f32 v29, -v37, v38, 1.0
	v_fmac_f32_e32 v38, v29, v38
	v_div_scale_f32 v29, vcc, 1.0, v36, 1.0
	v_mul_f32_e32 v33, v29, v38
	v_fma_f32 v39, -v37, v33, v29
	v_fmac_f32_e32 v33, v39, v38
	v_fma_f32 v29, -v37, v33, v29
	v_div_scale_f32 v37, s[4:5], v36, v36, v35
	v_rcp_f32_e32 v39, v37
	v_div_fmas_f32 v29, v29, v38, v33
	v_div_fixup_f32 v29, v29, v36, 1.0
	v_fma_f32 v29, v24, v29, v23
	v_fma_f32 v33, -v37, v39, 1.0
	v_fmac_f32_e32 v39, v33, v39
	v_div_scale_f32 v33, vcc, v35, v36, v35
	v_mul_f32_e32 v38, v33, v39
	v_fma_f32 v40, -v37, v38, v33
	v_fmac_f32_e32 v38, v40, v39
	v_cmp_gt_f32_e64 s[4:5], s74, v29
	v_fma_f32 v33, -v37, v38, v33
	v_div_fmas_f32 v33, v33, v39, v38
	v_cndmask_b32_e64 v37, 0, 32, s[4:5]
	v_ldexp_f32 v29, v29, v37
	v_log_f32_e32 v29, v29
	v_mul_f32_e32 v32, 0xbfb8aa3b, v32
	v_div_fixup_f32 v33, v33, v36, v35
	v_exp_f32_e32 v32, v32
	v_mul_f32_e32 v61, v24, v33
	v_mul_f32_e32 v33, 0x3f317217, v29
	v_fma_f32 v33, v29, s75, -v33
	v_fmac_f32_e32 v33, 0x3377d1cf, v29
	v_fmac_f32_e32 v33, 0x3f317217, v29
	v_cmp_lt_f32_e64 vcc, |v29|, s76
	v_add_f32_e32 v35, 1.0, v32
	s_waitcnt vmcnt(1)
; __device__ __forceinline__ float bf2f(bf16 b) { return __uint_as_float(((unsigned)b) << 16); }
; __device__ __forceinline__ void hgrn_x1_unit(const Args& a, int layer, int unit, LAS unsigned char* lds) {
;     ...
;     for (int i = 0; i < 8; ++i) {
;         const bf16* pr = PROJ + (tok0 + 8 * tq + i) * DIN + h * 128 + d;
;         q[i] = bf2f(pr[C_QA]); vv[i] = pr[C_IA];
;         float z = bf2f(pr[C_FA]); z = fminf(fmaxf(z, -30.f), 30.f);
;         const float e = __expf(-z), sp = 1.0f / (1.0f + e), sn = e / (1.0f + e);
;         const float f = lb + (1.0f - lb) * sp; kk[i] = (1.0f - lb) * sn;
;         run += __logf(f); c[i] = run;
;     }
;     __syncthreads();
;     TOT[tq * 128 + d] = run;
;     __syncthreads();
	v_lshlrev_b32_e32 v66, 16, v28
	v_cndmask_b32_e32 v29, v29, v33, vcc
	v_cndmask_b32_e64 v33, 0, v103, s[4:5]
	v_div_scale_f32 v36, s[4:5], v35, v35, 1.0
	s_mov_b32 s4, 0x26000
	s_nop 0
	v_add_co_u32_e64 v8, s[4:5], s4, v8
	v_rcp_f32_e32 v37, v36
	s_nop 0
	v_addc_co_u32_e64 v9, s[4:5], 0, v9, s[4:5]
	global_load_ushort v8, v[8:9], off offset:2048
	s_nop 0
	global_load_ushort v9, v[30:31], off
	v_sub_f32_e32 v29, v29, v33
	v_add_f32_e32 v62, v59, v29
	v_fma_f32 v29, -v36, v37, 1.0
	v_fmac_f32_e32 v37, v29, v37
	v_div_scale_f32 v29, vcc, 1.0, v35, 1.0
	v_div_scale_f32 v30, s[4:5], v35, v35, v32
	v_mul_f32_e32 v33, v29, v37
	v_rcp_f32_e32 v31, v30
	v_fma_f32 v38, -v36, v33, v29
	v_fmac_f32_e32 v33, v38, v37
	v_fma_f32 v29, -v36, v33, v29
	v_div_fmas_f32 v29, v29, v37, v33
	v_fma_f32 v33, -v30, v31, 1.0
	v_fmac_f32_e32 v31, v33, v31
	v_div_scale_f32 v33, vcc, v32, v35, v32
	v_div_fixup_f32 v29, v29, v35, 1.0
	v_mul_f32_e32 v36, v33, v31
	v_fma_f32 v37, -v30, v36, v33
	v_fma_f32 v29, v24, v29, v23
	v_fmac_f32_e32 v36, v37, v31
	v_cmp_gt_f32_e64 s[4:5], s74, v29
	v_fma_f32 v30, -v30, v36, v33
	v_div_fmas_f32 v30, v30, v31, v36
	v_cndmask_b32_e64 v33, 0, 32, s[4:5]
	v_ldexp_f32 v29, v29, v33
	v_log_f32_e32 v29, v29
	v_lshlrev_b32_e32 v31, 16, v34
	v_max_f32_e32 v31, v31, v31
	v_div_fixup_f32 v30, v30, v35, v32
	v_med3_f32 v31, v31, s73, v102
	v_mul_f32_e32 v64, v24, v30
	v_mul_f32_e32 v30, 0x3f317217, v29
	v_mul_f32_e32 v31, 0xbfb8aa3b, v31
	v_fma_f32 v30, v29, s75, -v30
	v_exp_f32_e32 v31, v31
	v_fmac_f32_e32 v30, 0x3377d1cf, v29
	v_fmac_f32_e32 v30, 0x3f317217, v29
	v_cmp_lt_f32_e64 vcc, |v29|, s76
	global_load_ushort v67, v[12:13], off
	s_nop 0
	v_cndmask_b32_e32 v29, v29, v30, vcc
	v_cndmask_b32_e64 v30, 0, v103, s[4:5]
	v_sub_f32_e32 v29, v29, v30
	v_add_f32_e32 v30, 1.0, v31
	v_div_scale_f32 v32, s[4:5], v30, v30, 1.0
	v_rcp_f32_e32 v33, v32
	v_add_f32_e32 v65, v62, v29
	s_barrier
	v_fma_f32 v12, -v32, v33, 1.0
	v_fmac_f32_e32 v33, v12, v33
	v_div_scale_f32 v12, vcc, 1.0, v30, 1.0
	v_mul_f32_e32 v13, v12, v33
	v_fma_f32 v28, -v32, v13, v12
	v_fmac_f32_e32 v13, v28, v33
	v_div_scale_f32 v28, s[4:5], v30, v30, v31
	v_rcp_f32_e32 v29, v28
	v_fma_f32 v12, -v32, v13, v12
	v_div_fmas_f32 v12, v12, v33, v13
	v_div_fixup_f32 v12, v12, v30, 1.0
	v_fma_f32 v13, -v28, v29, 1.0
	v_fmac_f32_e32 v29, v13, v29
	v_div_scale_f32 v13, vcc, v31, v30, v31
	v_mul_f32_e32 v32, v13, v29
	v_fma_f32 v33, -v28, v32, v13
	v_fma_f32 v12, v24, v12, v23
	v_fmac_f32_e32 v32, v33, v29
	v_cmp_gt_f32_e64 s[4:5], s74, v12
	v_fma_f32 v13, -v28, v32, v13
	v_div_fmas_f32 v13, v13, v29, v32
	v_cndmask_b32_e64 v28, 0, 32, s[4:5]
	v_ldexp_f32 v12, v12, v28
	s_waitcnt vmcnt(1)
	v_lshlrev_b32_e32 v9, 16, v9
	v_log_f32_e32 v12, v12
	v_max_f32_e32 v9, v9, v9
	v_med3_f32 v9, v9, s73, v102
	v_mul_f32_e32 v9, 0xbfb8aa3b, v9
	v_div_fixup_f32 v13, v13, v30, v31
	v_exp_f32_e32 v9, v9
	v_mul_f32_e32 v68, v24, v13
	v_mul_f32_e32 v13, 0x3f317217, v12
	v_fma_f32 v13, v12, s75, -v13
	v_fmac_f32_e32 v13, 0x3377d1cf, v12
	v_fmac_f32_e32 v13, 0x3f317217, v12
	v_cmp_lt_f32_e64 vcc, |v12|, s76
	v_add_f32_e32 v28, 1.0, v9
	v_lshlrev_b32_e32 v70, 16, v8
	v_cndmask_b32_e32 v12, v12, v13, vcc
	v_cndmask_b32_e64 v13, 0, v103, s[4:5]
	v_div_scale_f32 v29, s[4:5], v28, v28, 1.0
	v_rcp_f32_e32 v30, v29
	v_sub_f32_e32 v12, v12, v13
	v_add_f32_e32 v69, v65, v12
	v_lshl_add_u64 v[36:37], v[6:7], 0, v[4:5]
	v_fma_f32 v8, -v29, v30, 1.0
	v_fmac_f32_e32 v30, v8, v30
	v_div_scale_f32 v8, vcc, 1.0, v28, 1.0
	v_mul_f32_e32 v12, v8, v30
	v_fma_f32 v13, -v29, v12, v8
	v_fmac_f32_e32 v12, v13, v30
	v_div_scale_f32 v13, s[4:5], v28, v28, v9
	v_fma_f32 v8, -v29, v12, v8
	v_rcp_f32_e32 v29, v13
	v_div_fmas_f32 v8, v8, v30, v12
	v_div_fixup_f32 v8, v8, v28, 1.0
	v_fmac_f32_e32 v23, v24, v8
	v_fma_f32 v12, -v13, v29, 1.0
	v_cmp_gt_f32_e64 s[4:5], s74, v23
	v_fmac_f32_e32 v29, v12, v29
	v_div_scale_f32 v12, vcc, v9, v28, v9
	v_cndmask_b32_e64 v8, 0, 32, s[4:5]
	v_mul_f32_e32 v30, v12, v29
	v_ldexp_f32 v8, v23, v8
	v_fma_f32 v31, -v13, v30, v12
	v_log_f32_e32 v8, v8
	v_fmac_f32_e32 v30, v31, v29
	v_fma_f32 v12, -v13, v30, v12
	v_div_fmas_f32 v12, v12, v29, v30
	v_div_fixup_f32 v23, v12, v28, v9
	v_mul_f32_e32 v9, 0x3f317217, v8
	v_fma_f32 v9, v8, s75, -v9
	v_fmac_f32_e32 v9, 0x3377d1cf, v8
	v_fmac_f32_e32 v9, 0x3f317217, v8
	v_cmp_lt_f32_e64 vcc, |v8|, s76
	v_or_b32_e32 v4, 1, v2
	v_ashrrev_i32_e32 v5, 31, v4
	v_cndmask_b32_e32 v8, v8, v9, vcc
	v_cndmask_b32_e64 v9, 0, v103, s[4:5]
	v_sub_f32_e32 v8, v8, v9
	v_add_f32_e32 v9, v69, v8
	v_lshl_add_u32 v8, v14, 2, 0
	ds_write_b32 v8, v9
	v_lshl_add_u32 v8, v15, 2, 0
	s_waitcnt lgkmcnt(0)
	s_barrier
; #define LAS __attribute__((address_space(3)))
; __device__ __forceinline__ bf16 f2bf(float f) { return (bf16)(pk2(f, 0.f) & 0xffffu); }
; __device__ __forceinline__ void hgrn_x1_unit(const Args& a, int layer, int unit, LAS unsigned char* lds) {
;     ...
;     float off = 0.f, bl = 0.f;
; #pragma unroll
;     for (int g = 0; g < 4; ++g) { const float t = TOT[g * 128 + d]; bl += t; off += (g < tq) ? t : 0.f; }
;     unsigned kh[8];
; #pragma unroll
;     for (int i = 0; i < 8; ++i) {
;         const float bt = off + c[i];
;         const float qt = q[i] * __expf(bt), kh_ = kk[i] * __expf(bl - bt), kp = kk[i] * __expf(fminf(-bt, 80.f));
;         const int t = 8 * tq + i;
;         const bf16 qb = f2bf(qt);
;         *(LAS bf16*)(lds + HX_QL + t * 272 + d * 2) = qb;
;         *(LAS bf16*)(lds + HX_KP + t * 272 + d * 2) = f2bf(kp);
;         QT[(tok0 + t) * 1024 + h * 128 + d] = qb;
;         kh[i] = f2bf(kh_);
;     }
;     { u32x4 o; o.x = kh[0] | (kh[1] << 16); o.y = kh[2] | (kh[3] << 16); o.z = kh[4] | (kh[5] << 16); o.w = kh[6] | (kh[7] << 16); *(u32x4*)(KT + d * 32 + 8 * tq) = o;
	ds_read2st64_b32 v[12:13], v8 offset1:2
	ds_read2st64_b32 v[28:29], v8 offset0:4 offset1:6
	v_sub_u32_e32 v8, v8, v82
	v_mad_u64_u32 v[34:35], s[6:7], v16, s6, v[8:9]
	s_movk_i32 s6, 0x110
	s_nop 0
	v_mad_u64_u32 v[38:39], s[6:7], v4, s6, v[8:9]
	v_lshl_add_u64 v[4:5], v[4:5], 0, s[10:11]
	v_lshlrev_b64 v[4:5], 11, v[4:5]
	v_lshl_add_u64 v[40:41], v[6:7], 0, v[4:5]
	v_or_b32_e32 v4, 2, v2
	v_ashrrev_i32_e32 v5, 31, v4
	v_lshl_add_u64 v[4:5], v[4:5], 0, s[10:11]
	v_lshlrev_b64 v[4:5], 11, v[4:5]
	v_lshl_add_u64 v[42:43], v[6:7], 0, v[4:5]
	v_or_b32_e32 v4, 3, v2
	v_ashrrev_i32_e32 v5, 31, v4
	v_lshl_add_u64 v[4:5], v[4:5], 0, s[10:11]
	v_lshlrev_b64 v[4:5], 11, v[4:5]
	v_lshl_add_u64 v[44:45], v[6:7], 0, v[4:5]
	v_or_b32_e32 v4, 4, v2
	v_ashrrev_i32_e32 v5, 31, v4
	v_lshl_add_u64 v[4:5], v[4:5], 0, s[10:11]
	v_lshlrev_b64 v[4:5], 11, v[4:5]
	v_lshlrev_b32_e32 v63, 16, v46
	v_lshl_add_u64 v[46:47], v[6:7], 0, v[4:5]
	v_or_b32_e32 v4, 5, v2
	v_ashrrev_i32_e32 v5, 31, v4
	v_lshl_add_u64 v[4:5], v[4:5], 0, s[10:11]
	v_lshlrev_b64 v[4:5], 11, v[4:5]
	v_cmp_lt_i32_e32 vcc, 1, v16
	v_lshl_add_u64 v[48:49], v[6:7], 0, v[4:5]
	v_or_b32_e32 v4, 6, v2
	v_mul_f32_e32 v23, v24, v23
	s_waitcnt lgkmcnt(1)
	v_cndmask_b32_e32 v24, 0, v13, vcc
	v_cmp_lt_i32_e32 vcc, 2, v16
	v_ashrrev_i32_e32 v5, 31, v4
	v_lshl_add_u64 v[4:5], v[4:5], 0, s[10:11]
	s_waitcnt lgkmcnt(0)
	v_cndmask_b32_e32 v31, 0, v28, vcc
	v_cmp_lt_i32_e32 vcc, 3, v16
	v_lshlrev_b64 v[50:51], 11, v[4:5]
	v_add_f32_e32 v4, 0, v12
	v_cndmask_b32_e32 v33, 0, v29, vcc
	v_cmp_lt_i32_e32 vcc, 0, v16
	v_mov_b32_e32 v30, v13
	v_mov_b32_e32 v32, v28
	v_cndmask_b32_e32 v5, 0, v4, vcc
	v_add_f32_e32 v5, v5, v24
	v_pk_add_f32 v[4:5], v[4:5], v[30:31]
	v_mov_b32_e32 v8, v29
	v_pk_add_f32 v[12:13], v[4:5], v[32:33]
	s_lshl_b64 s[4:5], s[22:23], 13
	v_add_f32_e32 v22, v22, v13
	v_mul_f32_e32 v4, 0x3fb8aa3b, v22
	v_exp_f32_e32 v24, v4
	v_pk_add_f32 v[4:5], v[12:13], v[8:9]
	s_add_u32 s4, s8, s4
	v_sub_f32_e32 v8, v4, v22
	v_mul_f32_e32 v8, 0x3fb8aa3b, v8
	v_exp_f32_e32 v12, v8
	v_min_f32_e64 v8, -v22, s89
	v_mul_f32_e32 v8, 0x3fb8aa3b, v8
	v_exp_f32_e32 v22, v8
	v_mul_f32_e32 v20, v24, v20
	v_mul_f32_e32 v12, v21, v12
	v_cvt_pk_bf16_f32 v20, v20, v83
	v_mul_f32_e32 v21, v21, v22
	ds_write_b16 v34, v20 offset:2048
	v_cvt_pk_bf16_f32 v21, v21, v83
	v_and_b32_e32 v250, 0x7f, v0
	v_lshrrev_b32_e32 v251, 7, v0
	v_lshrrev_b32_e32 v252, 1, v251
	v_lshlrev_b32_e32 v252, 12, v252
	v_and_b32_e32 v251, 1, v251
	v_lshl_or_b32 v252, v251, 7, v252
	v_lshrrev_b32_e32 v251, 5, v250
	v_lshl_or_b32 v252, v251, 10, v252
	v_bfe_u32 v251, v250, 2, 2
	v_lshl_or_b32 v252, v251, 8, v252
	v_bfe_u32 v251, v250, 4, 1
	v_lshl_or_b32 v252, v251, 3, v252
	v_and_b32_e32 v251, 3, v250
	v_lshl_or_b32 v252, v251, 1, v252
	s_mul_i32 s100, s22, 0x2000
	v_add_u32_e32 v252, s100, v252
	v_add_u32_e32 v252, 0x45c82000, v252
	v_mov_b32_e32 v253, 0
	v_lshl_add_u64 v[252:253], s[8:9], 0, v[252:253]
	global_store_short v[252:253], v20, off
	v_add_f32_e32 v20, v53, v13
	ds_write_b16 v34, v21 offset:10752
	v_mul_f32_e32 v21, 0x3fb8aa3b, v20
	v_sub_f32_e32 v22, v4, v20
	v_min_f32_e64 v20, -v20, s89
	v_exp_f32_e32 v21, v21
	v_mul_f32_e32 v20, 0x3fb8aa3b, v20
	v_exp_f32_e32 v20, v20
	v_mul_f32_e32 v22, 0x3fb8aa3b, v22
	v_exp_f32_e32 v22, v22
	v_mul_f32_e32 v19, v21, v19
	v_cvt_pk_bf16_f32 v12, v12, v83
	v_mul_f32_e32 v20, v52, v20
	v_cvt_pk_bf16_f32 v19, v19, v83
	ds_write_b16 v38, v19 offset:2048
	v_cvt_pk_bf16_f32 v20, v20, v83
	global_store_short v[252:253], v19, off offset:16
	v_add_f32_e32 v19, v56, v13
	v_mul_f32_e32 v21, v52, v22
	ds_write_b16 v38, v20 offset:10752
	v_mul_f32_e32 v20, 0x3fb8aa3b, v19
	v_sub_f32_e32 v22, v4, v19
	v_min_f32_e64 v19, -v19, s89
	v_exp_f32_e32 v20, v20
	v_mul_f32_e32 v19, 0x3fb8aa3b, v19
	v_mul_f32_e32 v22, 0x3fb8aa3b, v22
	v_exp_f32_e32 v19, v19
	v_exp_f32_e32 v22, v22
	v_mul_f32_e32 v20, v20, v54
	v_cvt_pk_bf16_f32 v21, v21, v83
	v_mul_f32_e32 v19, v55, v19
	v_cvt_pk_bf16_f32 v20, v20, v83
	v_mul_f32_e32 v22, v55, v22
	ds_write_b16 v38, v20 offset:2320
	v_cvt_pk_bf16_f32 v19, v19, v83
	global_store_short v[252:253], v20, off offset:32
	v_add_f32_e32 v20, v59, v13
	ds_write_b16 v38, v19 offset:11024
	v_cvt_pk_bf16_f32 v19, v22, v83
	v_mul_f32_e32 v22, 0x3fb8aa3b, v20
	v_sub_f32_e32 v24, v4, v20
; #define LAS __attribute__((address_space(3)))
; __device__ __forceinline__ bf16 f2bf(float f) { return (bf16)(pk2(f, 0.f) & 0xffffu); }
; __device__ __forceinline__ void hgrn_x1_unit(const Args& a, int layer, int unit, LAS unsigned char* lds) {
;     ...
;     for (int i = 0; i < 8; ++i) {
;         const float bt = off + c[i];
;         const float qt = q[i] * __expf(bt), kh_ = kk[i] * __expf(bl - bt), kp = kk[i] * __expf(fminf(-bt, 80.f));
;         const int t = 8 * tq + i;
;         const bf16 qb = f2bf(qt);
;         *(LAS bf16*)(lds + HX_QL + t * 272 + d * 2) = qb;
;         *(LAS bf16*)(lds + HX_KP + t * 272 + d * 2) = f2bf(kp);
;         QT[(tok0 + t) * 1024 + h * 128 + d] = qb;
;         kh[i] = f2bf(kh_);
;     }
;     { u32x4 o; o.x = kh[0] | (kh[1] << 16); o.y = kh[2] | (kh[3] << 16); o.z = kh[4] | (kh[5] << 16); o.w = kh[6] | (kh[7] << 16); *(u32x4*)(KT + d * 32 + 8 * tq) = o;
;       u32x4 w; w.x = vv[0] | ((unsigned)vv[1] << 16); w.y = vv[2] | ((unsigned)vv[3] << 16); w.z = vv[4] | ((unsigned)vv[5] << 16); w.w = vv[6] | ((unsigned)vv[7] << 16);
;       *(u32x4*)(VT + d * 32 + 8 * tq) = w; *(LAS u32x4*)(lds + HX_VL + d * 80 + 16 * tq) = w; }
;     if (tq == 0) DEC[d] = __expf(bl);
	v_min_f32_e64 v20, -v20, s89
	v_mul_f32_e32 v20, 0x3fb8aa3b, v20
	v_exp_f32_e32 v22, v22
	v_exp_f32_e32 v20, v20
	v_mul_f32_e32 v24, 0x3fb8aa3b, v24
	v_exp_f32_e32 v24, v24
	v_mul_f32_e32 v22, v22, v57
	v_mul_f32_e32 v20, v58, v20
	v_cvt_pk_bf16_f32 v22, v22, v83
	ds_write_b16 v38, v22 offset:2592
	v_cvt_pk_bf16_f32 v20, v20, v83
	ds_write_b16 v38, v20 offset:11296
	v_add_f32_e32 v20, v62, v13
	global_store_short v[252:253], v22, off offset:48
	v_mul_f32_e32 v22, 0x3fb8aa3b, v20
	v_sub_f32_e32 v28, v4, v20
	v_min_f32_e64 v20, -v20, s89
	v_exp_f32_e32 v22, v22
	v_mul_f32_e32 v20, 0x3fb8aa3b, v20
	v_mul_f32_e32 v28, 0x3fb8aa3b, v28
	v_exp_f32_e32 v20, v20
	v_exp_f32_e32 v28, v28
	v_mul_f32_e32 v24, v58, v24
	v_mul_f32_e32 v22, v22, v60
	v_cvt_pk_bf16_f32 v24, v24, v83
	v_mul_f32_e32 v20, v61, v20
	v_cvt_pk_bf16_f32 v22, v22, v83
	v_mul_f32_e32 v28, v61, v28
	ds_write_b16 v38, v22 offset:2864
	v_cvt_pk_bf16_f32 v20, v20, v83
	global_store_short v[252:253], v22, off offset:64
	v_add_f32_e32 v22, v65, v13
	ds_write_b16 v38, v20 offset:11568
	v_cvt_pk_bf16_f32 v20, v28, v83
	v_mul_f32_e32 v28, 0x3fb8aa3b, v22
	v_sub_f32_e32 v29, v4, v22
	v_min_f32_e64 v22, -v22, s89
	v_mul_f32_e32 v22, 0x3fb8aa3b, v22
	v_exp_f32_e32 v28, v28
	v_exp_f32_e32 v22, v22
	v_add_f32_e32 v13, v69, v13
	v_mul_f32_e32 v29, 0x3fb8aa3b, v29
	v_mul_f32_e32 v28, v28, v63
	v_mul_f32_e32 v22, v64, v22
	v_cvt_pk_bf16_f32 v28, v28, v83
	ds_write_b16 v38, v28 offset:3136
	v_cvt_pk_bf16_f32 v22, v22, v83
	ds_write_b16 v38, v22 offset:11840
	global_store_short v[252:253], v28, off offset:80
	v_mul_f32_e32 v22, 0x3fb8aa3b, v13
	v_sub_f32_e32 v28, v4, v13
	v_min_f32_e64 v13, -v13, s89
	v_mul_f32_e32 v13, 0x3fb8aa3b, v13
	v_exp_f32_e32 v29, v29
	v_exp_f32_e32 v22, v22
	v_exp_f32_e32 v13, v13
	v_lshl_add_u64 v[8:9], v[6:7], 0, v[50:51]
	v_mul_f32_e32 v29, v64, v29
	v_mul_f32_e32 v22, v22, v66
	v_mul_f32_e32 v13, v68, v13
	v_mul_f32_e32 v28, 0x3fb8aa3b, v28
	v_cvt_pk_bf16_f32 v29, v29, v83
	v_cvt_pk_bf16_f32 v22, v22, v83
	ds_write_b16 v38, v22 offset:3408
	v_cvt_pk_bf16_f32 v13, v13, v83
	v_exp_f32_e32 v28, v28
	ds_write_b16 v38, v13 offset:12112
	global_store_short v[252:253], v22, off offset:96
	v_mul_f32_e32 v9, 0x3fb8aa3b, v5
	v_sub_f32_e32 v13, v4, v5
	v_min_f32_e64 v5, -v5, s89
	v_exp_f32_e32 v9, v9
	v_mul_f32_e32 v13, 0x3fb8aa3b, v13
	v_mul_f32_e32 v5, 0x3fb8aa3b, v5
	v_exp_f32_e32 v13, v13
	v_exp_f32_e32 v5, v5
	v_mul_f32_e32 v28, v68, v28
	v_cvt_pk_bf16_f32 v8, v28, v83
	v_mul_f32_e32 v9, v9, v70
	v_and_b32_e32 v22, 0xffff, v8
	v_or_b32_e32 v8, 7, v2
	v_mul_f32_e32 v13, v23, v13
	v_mul_f32_e32 v5, v23, v5
	v_cvt_pk_bf16_f32 v23, v9, v83
	v_ashrrev_i32_e32 v9, 31, v8
	v_lshl_add_u64 v[8:9], v[8:9], 0, s[10:11]
	v_lshlrev_b64 v[8:9], 11, v[8:9]
	s_addc_u32 s5, s9, s5
	v_and_b32_e32 v19, 0xffff, v19
	v_lshl_add_u64 v[6:7], v[6:7], 0, v[8:9]
	v_lshlrev_b32_e32 v82, 6, v15
	ds_write_b16 v38, v23 offset:3680
	v_cvt_pk_bf16_f32 v5, v5, v83
	global_store_short v[252:253], v23, off offset:112
	v_perm_b32 v8, v26, v11, s90
	v_perm_b32 v6, v17, v18, s90
	v_lshl_or_b32 v11, v24, 16, v19
	v_lshl_add_u64 v[18:19], s[4:5], 0, v[82:83]
	v_lshl_add_u64 v[2:3], v[2:3], 1, v[18:19]
	v_add_co_u32_e32 v18, vcc, s91, v2
	s_waitcnt vmcnt(8)
	v_perm_b32 v9, v27, v67, s90
	v_addc_co_u32_e32 v19, vcc, 0, v3, vcc
	v_add_co_u32_e32 v2, vcc, 0x47c82000, v2
	v_perm_b32 v7, v25, v10, s90
	s_nop 0
	v_addc_co_u32_e32 v3, vcc, 0, v3, vcc
	v_and_b32_e32 v12, 0xffff, v12
	v_and_b32_e32 v20, 0xffff, v20
	ds_write_b16 v38, v5 offset:12384
	v_cvt_pk_bf16_f32 v5, v13, v83
	global_store_dwordx4 v[2:3], v[6:9], off
	v_mul_u32_u24_e32 v2, 0x50, v15
	v_lshlrev_b32_e32 v3, 4, v16
	v_lshl_or_b32 v10, v21, 16, v12
	v_lshl_or_b32 v12, v29, 16, v20
	v_lshl_or_b32 v13, v5, 16, v22
	v_add3_u32 v2, 0, v2, v3
	v_cmp_gt_u32_e32 vcc, s93, v14
	global_store_dwordx4 v[18:19], v[10:13], off
	ds_write_b128 v2, v[6:9] offset:19456
	s_and_saveexec_b64 s[4:5], vcc
	s_cbranch_execz .LBB0_326
	s_lshl_b64 s[6:7], s[22:23], 9
	s_add_u32 s6, s8, s6
	v_mul_f32_e32 v4, 0x3fb8aa3b, v4
	s_addc_u32 s7, s9, s7
	v_lshlrev_b32_e32 v82, 2, v15
	v_exp_f32_e32 v4, v4
	v_lshl_add_u64 v[2:3], s[6:7], 0, v[82:83]
	v_add_co_u32_e32 v2, vcc, 0x48c82000, v2
	s_nop 1
	v_addc_co_u32_e32 v3, vcc, 0, v3, vcc
	global_store_dword v[2:3], v4, off

; __device__ __forceinline__ void hgrn_x2_unit(const Args& a, int unit) {
;     ...
;     const int vs = unit & 7, h = (unit >> 3) & 7, b = unit >> 6;
;     const bf16* QT = (const bf16*)(ws + WS_HQT); float* OI = (float*)(ws + WS_HOI);
;     const int fr = lane & 15, fg = lane >> 4;
;     f32x4 S[8];
; #pragma unroll
;     for (int i = 0; i < 8; ++i) S[i] = (f32x4){0.f, 0.f, 0.f, 0.f};
; #pragma unroll 1
;     for (int blk = 0; blk < SEQ / HB; ++blk) {
;         const int u = (b * 8 + h) * 64 + blk; const size_t tok0 = (size_t)b * SEQ + blk * HB;
;         const bf16* KT = (const bf16*)(ws + WS_HKT) + (size_t)u * 4096; const bf16* VT = (const bf16*)(ws + WS_HVT) + (size_t)u * 4096; const float* DEC = (const float*)(ws + WS_HDEC) + (size_t)u * 128;
;         FragU Aq[2][4]; f32x4 o[2]; FragU Ak[8]; f32x4 dc[8]; FragU Bv;
; #pragma unroll
;         for (int mt = 0; mt < 2; ++mt) { const bf16* qr = QT + (tok0 + 16 * mt + fr) * 1024 + h * 128;
; #pragma unroll
;             for (int ks = 0; ks < 4; ++ks) { Aq[mt][ks].h[0] = *(const u32x2*)(qr + 32 * ks + 4 * fg); Aq[mt][ks].h[1] = *(const u32x2*)(qr + 32 * ks + 16 + 4 * fg); }
; #pragma unroll
;             for (int r = 0; r < 4; ++r) o[mt][r] = OI[(tok0 + 16 * mt + 4 * fg + r) * 1024 + h * 128 + 16 * vs + fr]; }
; #pragma unroll
;         for (int dt = 0; dt < 8; ++dt) { Ak[dt].u = *(const u32x4*)(KT + (16 * dt + fr) * 32 + 8 * fg); dc[dt] = *(const f32x4*)(DEC + 16 * dt + 4 * fg); }
;         Bv.u = *(const u32x4*)(VT + (16 * vs + fr) * 32 + 8 * fg);
.LBB0_733:
	s_andn2_b64 vcc, exec, s[6:7]
	s_cbranch_vccnz .LBB0_736
	s_lshl_b32 s4, s60, 1
	s_add_i32 s14, s2, s4
	v_mov_b32_e32 v1, v0
	s_mov_b64 s[4:5], 0
	s_ashr_i32 s8, s14, 6
	s_load_dwordx2 s[6:7], s[0:1], 0xd0
	s_ashr_i32 s9, s8, 31
	v_and_b32_e32 v4, 15, v1
	v_bfe_u32 v1, v1, 4, 2
	s_lshl_b64 s[10:11], s[8:9], 23
	s_bfe_u32 s15, s14, 0x30003
	v_lshl_or_b32 v2, v1, 14, s10
	s_and_b32 s14, s14, 7
	v_lshl_or_b32 v2, s15, 9, v2
	s_lshl_b32 s10, s14, 6
	v_lshlrev_b32_e32 v3, 2, v4
	s_lshl_b32 s16, s8, 9
	v_or3_b32 v2, v2, s10, v3
	v_mov_b32_e32 v3, s11
	s_lshl_b64 s[8:9], s[8:9], 22
	s_lshl_b32 s17, s15, 6
	v_lshlrev_b32_e32 v5, 3, v1
	s_waitcnt vmcnt(8) lgkmcnt(0)
	v_lshl_add_u64 v[46:47], s[6:7], 0, v[2:3]
	v_lshl_or_b32 v2, v4, 11, s8
	s_lshl_b32 s8, s15, 8
	v_or3_b32 v2, v2, s8, v5
	s_or_b32 s8, s16, s17
	v_mov_b32_e32 v3, s9
	s_ashr_i32 s9, s8, 31
	v_and_b32_e32 v250, 63, v0
	v_lshlrev_b32_e32 v250, 4, v250
	s_mul_i32 s100, s8, 0x2000
	v_add_u32_e32 v250, s100, v250
	v_mov_b32_e32 v251, 0
	v_lshl_add_u64 v[48:49], s[6:7], 0, v[250:251]
	s_lshl_b64 s[10:11], s[8:9], 13
	v_lshlrev_b32_e32 v2, 4, v1
	v_or_b32_e32 v1, s10, v2
	s_lshl_b32 s10, s14, 10
	v_lshlrev_b32_e32 v8, 6, v4
	v_or3_b32 v4, s10, v8, v1
	v_mov_b32_e32 v5, s11
	v_lshl_add_u64 v[6:7], s[6:7], 0, v[4:5]
	v_or_b32_e32 v4, v1, v8
	s_lshl_b64 s[8:9], s[8:9], 9
	v_lshl_add_u64 v[52:53], s[6:7], 0, v[4:5]
	s_add_u32 s6, s6, s8
	v_mov_b32_e32 v3, 0
	s_addc_u32 s7, s7, s9
	s_mov_b64 s[10:11], 0x47c82000
	v_lshl_add_u64 v[4:5], s[6:7], 0, v[2:3]
	s_mov_b64 s[6:7], 0x48c82100
	v_lshl_add_u64 v[50:51], v[6:7], 0, s[10:11]
	v_lshl_add_u64 v[54:55], v[4:5], 0, s[6:7]
	s_mov_b32 s16, 64
	s_mov_b32 s17, 0x45c82000
	s_mov_b32 s18, 0x48d83000
	s_mov_b32 s19, 0x48d85000
	s_mov_b32 s20, 0x45c83000
	s_mov_b32 s21, 0x48d93000
	s_mov_b32 s22, 0x48d95000
	s_mov_b32 s23, 0x46c82000
	s_mov_b32 s24, 0x46c83000
	s_mov_b64 s[6:7], 0x20000
	s_mov_b64 s[8:9], 0x2000
	s_mov_b64 s[10:11], 0x2000
	s_mov_b64 s[14:15], 0x200
	v_mov_b32_e32 v2, v3
	v_mov_b32_e32 v4, v3
	v_mov_b32_e32 v5, v3
	v_mov_b32_e32 v6, v3
	v_mov_b32_e32 v7, v3
	v_mov_b32_e32 v8, v3
	v_mov_b32_e32 v9, v3
	v_mov_b32_e32 v10, v3
	v_mov_b32_e32 v11, v3
	v_mov_b32_e32 v12, v3
	v_mov_b32_e32 v13, v3
	v_mov_b32_e32 v14, v3
	v_mov_b32_e32 v15, v3
	v_mov_b32_e32 v16, v3
	v_mov_b32_e32 v17, v3
	v_mov_b32_e32 v18, v3
	v_mov_b32_e32 v19, v3
	v_mov_b32_e32 v20, v3
	v_mov_b32_e32 v21, v3
	v_mov_b32_e32 v22, v3
	v_mov_b32_e32 v23, v3
	v_mov_b32_e32 v24, v3
	v_mov_b32_e32 v25, v3
	v_mov_b32_e32 v26, v3
	v_mov_b32_e32 v27, v3
	v_mov_b32_e32 v28, v3
	v_mov_b32_e32 v29, v3
	v_mov_b32_e32 v30, v3
	v_mov_b32_e32 v31, v3
	v_mov_b32_e32 v32, v3
	v_mov_b32_e32 v33, v3
; __device__ __forceinline__ unsigned pk2(float lo, float hi) { unsigned r; asm volatile("v_cvt_pk_bf16_f32 %0, %1, %2" : "=v"(r) : "v"(lo), "v"(hi)); return r; }
; __device__ __forceinline__ f32x4 mfma16(bf16x8 a, bf16x8 b, f32x4 c) { return __builtin_amdgcn_mfma_f32_16x16x32_bf16(a, b, c, 0, 0, 0); }
; __device__ __forceinline__ void hgrn_x2_unit(const Args& a, int unit) {
;     ...
;     for (int blk = 0; blk < SEQ / HB; ++blk) {
;         const int u = (b * 8 + h) * 64 + blk; const size_t tok0 = (size_t)b * SEQ + blk * HB;
;         const bf16* KT = (const bf16*)(ws + WS_HKT) + (size_t)u * 4096; const bf16* VT = (const bf16*)(ws + WS_HVT) + (size_t)u * 4096; const float* DEC = (const float*)(ws + WS_HDEC) + (size_t)u * 128;
;         FragU Aq[2][4]; f32x4 o[2]; FragU Ak[8]; f32x4 dc[8]; FragU Bv;
; #pragma unroll
;         for (int mt = 0; mt < 2; ++mt) { const bf16* qr = QT + (tok0 + 16 * mt + fr) * 1024 + h * 128;
; #pragma unroll
;             for (int ks = 0; ks < 4; ++ks) { Aq[mt][ks].h[0] = *(const u32x2*)(qr + 32 * ks + 4 * fg); Aq[mt][ks].h[1] = *(const u32x2*)(qr + 32 * ks + 16 + 4 * fg); }
; #pragma unroll
;             for (int r = 0; r < 4; ++r) o[mt][r] = OI[(tok0 + 16 * mt + 4 * fg + r) * 1024 + h * 128 + 16 * vs + fr]; }
; #pragma unroll
;         for (int dt = 0; dt < 8; ++dt) { Ak[dt].u = *(const u32x4*)(KT + (16 * dt + fr) * 32 + 8 * fg); dc[dt] = *(const f32x4*)(DEC + 16 * dt + 4 * fg); }
;         Bv.u = *(const u32x4*)(VT + (16 * vs + fr) * 32 + 8 * fg);
; #pragma unroll
;         for (int ks = 0; ks < 4; ++ks) { FragU Sb; Sb.u.x = pk2(S[2 * ks][0], S[2 * ks][1]); Sb.u.y = pk2(S[2 * ks][2], S[2 * ks][3]); Sb.u.z = pk2(S[2 * ks + 1][0], S[2 * ks + 1][1]); Sb.u.w = pk2(S[2 * ks + 1][2], S[2 * ks + 1][3]);
;             o[0] = mfma16(Aq[0][ks].v, Sb.v, o[0]); o[1] = mfma16(Aq[1][ks].v, Sb.v, o[1]); }
; #pragma unroll
;         for (int mt = 0; mt < 2; ++mt)
; #pragma unroll
;             for (int r = 0; r < 4; ++r) OI[(tok0 + 16 * mt + 4 * fg + r) * 1024 + h * 128 + 16 * vs + fr] = o[mt][r];
; #pragma unroll
;         for (int dt = 0; dt < 8; ++dt) S[dt] = mfma16(Ak[dt].v, Bv.v, S[dt] * dc[dt]);
.LBB0_735:
	v_lshl_add_u64 v[34:35], v[48:49], 0, s[4:5]
	v_add_co_u32_e32 v120, vcc, s17, v34
	v_lshl_add_u64 v[36:37], v[46:47], 0, s[4:5]
	s_nop 0
	v_addc_co_u32_e32 v121, vcc, 0, v35, vcc
	v_add_co_u32_e32 v56, vcc, s18, v36
	v_lshl_add_u64 v[40:41], v[52:53], 0, s[4:5]
	s_nop 0
	v_addc_co_u32_e32 v57, vcc, 0, v37, vcc
	v_add_co_u32_e32 v58, vcc, s19, v36
	v_lshl_add_u64 v[38:39], v[54:55], 0, s[4:5]
	s_nop 0
	v_addc_co_u32_e32 v59, vcc, 0, v37, vcc
	v_add_co_u32_e32 v122, vcc, s20, v34
	v_lshl_add_u64 v[156:157], v[50:51], 0, s[4:5]
	s_nop 0
	v_addc_co_u32_e32 v123, vcc, 0, v35, vcc
	v_add_co_u32_e32 v60, vcc, s21, v36
	s_add_i32 s16, s16, -1
	s_nop 0
	v_addc_co_u32_e32 v61, vcc, 0, v37, vcc
	v_add_co_u32_e32 v62, vcc, s22, v36
	v_lshl_add_u64 v[46:47], v[46:47], 0, s[6:7]
	s_nop 0
	v_addc_co_u32_e32 v63, vcc, 0, v37, vcc
	v_add_co_u32_e32 v132, vcc, s23, v40
	v_lshl_add_u64 v[48:49], v[48:49], 0, s[8:9]
	s_nop 0
	v_addc_co_u32_e32 v133, vcc, 0, v41, vcc
	v_add_co_u32_e32 v152, vcc, s24, v40
	v_lshl_add_u64 v[50:51], v[50:51], 0, s[10:11]
	s_nop 0
	v_addc_co_u32_e32 v153, vcc, 0, v41, vcc
	global_load_dwordx4 v[64:67], v[38:39], off offset:-256
	global_load_dwordx4 v[68:71], v[38:39], off offset:-192
	global_load_dwordx4 v[72:75], v[38:39], off offset:-128
	global_load_dwordx4 v[76:79], v[38:39], off offset:-64
	global_load_dwordx4 v[80:83], v[38:39], off
	global_load_dwordx4 v[84:87], v[38:39], off offset:64
	global_load_dwordx4 v[88:91], v[38:39], off offset:128
	global_load_dwordx4 v[92:95], v[38:39], off offset:192
	global_load_dwordx4 v[96:99], v[120:121], off
	s_nop 0
	global_load_dwordx4 v[100:103], v[120:121], off offset:1024
	s_nop 0
	global_load_dwordx4 v[104:107], v[120:121], off offset:2048
	s_nop 0
	global_load_dwordx4 v[34:37], v[120:121], off offset:3072
	s_nop 0
	global_load_dwordx4 v[108:111], v[122:123], off
	s_nop 0
	global_load_dwordx4 v[112:115], v[122:123], off offset:1024
	s_nop 0
	global_load_dwordx4 v[42:45], v[122:123], off offset:2048
	s_nop 0
	global_load_dwordx4 v[38:41], v[122:123], off offset:3072
	s_nop 0
	global_load_dword v116, v[56:57], off offset:-4096
	global_load_dword v117, v[56:57], off
	global_load_dword v118, v[58:59], off offset:-4096
	global_load_dword v119, v[58:59], off
	global_load_dword v120, v[60:61], off offset:-4096
	global_load_dword v121, v[60:61], off
	global_load_dword v122, v[62:63], off offset:-4096
	global_load_dword v123, v[62:63], off
	global_load_dwordx4 v[124:127], v[132:133], off offset:1024
	global_load_dwordx4 v[128:131], v[132:133], off offset:2048
	s_nop 0
	global_load_dwordx4 v[132:135], v[132:133], off offset:3072
	s_nop 0
	global_load_dwordx4 v[136:139], v[152:153], off offset:-4096
	global_load_dwordx4 v[140:143], v[152:153], off
	global_load_dwordx4 v[144:147], v[152:153], off offset:1024
	global_load_dwordx4 v[148:151], v[152:153], off offset:2048
	s_nop 0
	global_load_dwordx4 v[152:155], v[152:153], off offset:3072
	s_nop 0
	global_load_dwordx4 v[156:159], v[156:157], off
	v_cvt_pk_bf16_f32 v160, v2, v3
	v_cvt_pk_bf16_f32 v161, v4, v5
	v_cvt_pk_bf16_f32 v162, v6, v7
	v_cvt_pk_bf16_f32 v163, v8, v9
	v_cvt_pk_bf16_f32 v164, v10, v11
	v_cvt_pk_bf16_f32 v165, v12, v13
	v_cvt_pk_bf16_f32 v166, v14, v15
	v_cvt_pk_bf16_f32 v167, v16, v17
	v_lshl_add_u64 v[52:53], v[52:53], 0, s[10:11]
	v_lshl_add_u64 v[54:55], v[54:55], 0, s[14:15]
	s_cmp_eq_u32 s16, 0
	s_waitcnt vmcnt(13)
	v_mfma_f32_16x16x32_bf16 v[96:99], v[96:99], v[160:163], v[116:119]
	v_mul_f32_e64 v6, v6, v68
	v_mul_f32_e64 v7, v7, v69
	v_pk_mul_f32 v[8:9], v[8:9], v[70:71]
	v_cvt_pk_bf16_f32 v116, v18, v19
	s_waitcnt vmcnt(9)
	v_mfma_f32_16x16x32_bf16 v[108:111], v[108:111], v[160:163], v[120:123]
	v_cvt_pk_bf16_f32 v117, v20, v21
	v_cvt_pk_bf16_f32 v118, v22, v23
	v_mul_f32_e64 v10, v10, v72
	v_mul_f32_e64 v11, v11, v73
	v_mfma_f32_16x16x32_bf16 v[68:71], v[100:103], v[164:167], v[96:99]
	v_mul_f32_e64 v12, v12, v74
	v_mul_f32_e64 v13, v13, v75
	v_cvt_pk_bf16_f32 v119, v24, v25
	v_pk_mul_f32 v[2:3], v[2:3], v[64:65]
	v_mfma_f32_16x16x32_bf16 v[72:75], v[112:115], v[164:167], v[108:111]
	v_mul_f32_e64 v4, v4, v66
	v_mul_f32_e64 v5, v5, v67
	v_pk_mul_f32 v[14:15], v[14:15], v[76:77]
	v_pk_mul_f32 v[16:17], v[16:17], v[78:79]
	v_mfma_f32_16x16x32_bf16 v[68:71], v[104:107], v[116:119], v[68:71]
	v_cvt_pk_bf16_f32 v64, v26, v27
	v_mul_f32_e64 v18, v18, v80
	v_mul_f32_e64 v19, v19, v81
	v_pk_mul_f32 v[20:21], v[20:21], v[82:83]
	v_cvt_pk_bf16_f32 v65, v28, v29
	v_pk_mul_f32 v[22:23], v[22:23], v[84:85]
	v_pk_mul_f32 v[24:25], v[24:25], v[86:87]
	v_cvt_pk_bf16_f32 v66, v30, v31
	v_pk_mul_f32 v[26:27], v[26:27], v[88:89]
	v_pk_mul_f32 v[28:29], v[28:29], v[90:91]
	v_cvt_pk_bf16_f32 v67, v32, v33
	v_pk_mul_f32 v[30:31], v[30:31], v[92:93]
	v_pk_mul_f32 v[32:33], v[32:33], v[94:95]
	s_waitcnt vmcnt(0)
	v_mfma_f32_16x16x32_bf16 v[2:5], v[136:139], v[156:159], v[2:5]
	v_mfma_f32_16x16x32_bf16 v[6:9], v[124:127], v[156:159], v[6:9]
	v_mfma_f32_16x16x32_bf16 v[10:13], v[128:131], v[156:159], v[10:13]
	v_mfma_f32_16x16x32_bf16 v[14:17], v[132:135], v[156:159], v[14:17]
	v_mfma_f32_16x16x32_bf16 v[18:21], v[140:143], v[156:159], v[18:21]
	v_mfma_f32_16x16x32_bf16 v[22:25], v[144:147], v[156:159], v[22:25]
	v_mfma_f32_16x16x32_bf16 v[26:29], v[148:151], v[156:159], v[26:29]
	v_mfma_f32_16x16x32_bf16 v[30:33], v[152:155], v[156:159], v[30:33]
	v_mfma_f32_16x16x32_bf16 v[42:45], v[42:45], v[116:119], v[72:75]
	v_mfma_f32_16x16x32_bf16 v[34:37], v[34:37], v[64:67], v[68:71]
	v_mfma_f32_16x16x32_bf16 v[38:41], v[38:41], v[64:67], v[42:45]
	s_nop 6
	global_store_dword v[56:57], v34, off offset:-4096
	global_store_dword v[56:57], v35, off
	global_store_dword v[58:59], v36, off offset:-4096
	global_store_dword v[58:59], v37, off
	global_store_dword v[60:61], v38, off offset:-4096
	global_store_dword v[60:61], v39, off
	global_store_dword v[62:63], v40, off offset:-4096
	global_store_dword v[62:63], v41, off
	s_cbranch_scc0 .LBB0_735

; #define LAS __attribute__((address_space(3)))
; __device__ __forceinline__ void hgrn_x1_unit(const Args& a, int layer, int unit, LAS unsigned char* lds) {
;     int tid = threadIdx.x; asm volatile("" : "+v"(tid)); const int lane = tid & 63; const int wave = __builtin_amdgcn_readfirstlane(tid >> 6);
;     size_t wz_ = 0; asm volatile("" : "+s"(wz_)); unsigned char* ws = a.ws + wz_;
;     const int blk = unit & 63, h = (unit >> 6) & 7, b = unit >> 9;
;     const bf16* PROJ = (const bf16*)(ws + WS_PROJ);
;     bf16* QT = (bf16*)(ws + WS_HQT); bf16* KT = (bf16*)(ws + WS_HKT) + (size_t)unit * 4096; bf16* VT = (bf16*)(ws + WS_HVT) + (size_t)unit * 4096;
;     float* DEC = (float*)(ws + WS_HDEC) + (size_t)unit * 128; float* OI = (float*)(ws + WS_HOI);
;     LAS float* TOT = (LAS float*)(lds + HX_TOT);
;     const size_t tok0 = (size_t)b * SEQ + blk * HB;
;     const int d = tid & 127, tq = tid >> 7;
;     const float lb = ((const float*)(ws + WS_LB))[layer * 1024 + h * 128 + d];
;     float q[8], kk[8], c[8]; unsigned short vv[8];
;     float run = 0.f;
; #pragma unroll
;     for (int i = 0; i < 8; ++i) {
;         const bf16* pr = PROJ + (tok0 + 8 * tq + i) * DIN + h * 128 + d;
;         q[i] = bf2f(pr[C_QA]); vv[i] = pr[C_IA];
;         float z = bf2f(pr[C_FA]); z = fminf(fmaxf(z, -30.f), 30.f);
;         const float e = __expf(-z), sp = 1.0f / (1.0f + e), sn = e / (1.0f + e);
;         const float f = lb + (1.0f - lb) * sp; kk[i] = (1.0f - lb) * sn;
;         run += __logf(f); c[i] = run;
; template <int LAYER>
; __device__ __forceinline__ void layer_phases(const Args& args, LAS unsigned char* lds, const XcdBarrier& bar, int lo, int hi) {
;     ...
;         for (;;) {
;             __syncthreads();
;             if (threadIdx.x == 0) *slot = (int)__hip_atomic_fetch_add(ctr, 1u, __ATOMIC_RELAXED, __HIP_MEMORY_SCOPE_AGENT);
;             __syncthreads();
;             const int it = __builtin_amdgcn_readfirstlane(*slot);
;             if (it >= 256 + 1024 + 2048) break;
;             if (it < 256) s5_unit(args, LAYER, it, lds);
;             else if (it < 1280) { const int j = it - 256, n = 31 - (j >> 5), b = (j >> 3) & 3, hp = j & 7, n0_ = (b & 1) ? 31 - n : n; attn_item(args, LAYER, b * 256 + n0_ * 8 + hp, lds); }
;             else hgrn_x1_unit(args, LAYER, it - 1280, lds);
.LBB0_1388:
	s_or_b64 exec, exec, s[4:5]
	s_waitcnt lgkmcnt(0)
	s_barrier
	ds_read_b32 v2, v1
	s_mov_b64 s[4:5], -1
	s_waitcnt lgkmcnt(0)
	v_readfirstlane_b32 s2, v2
	s_cmpk_gt_i32 s2, 0xcff
	s_cbranch_scc1 .LBB0_1383
	s_cmpk_gt_i32 s2, 0xff
	s_cbranch_scc0 .LBB0_1416
	s_cmpk_gt_u32 s2, 0x4ff
	s_cbranch_scc0 .LBB0_1394
	s_add_i32 s12, s2, 0xfffffb00
	v_mov_b32_e32 v14, v0
	s_mov_b64 s[4:5], 0
	s_add_u32 s42, s10, s4
	s_addc_u32 s43, s11, s5
	s_lshl_b32 s4, s12, 2
	s_lshl_b32 s5, s12, 5
	s_and_b32 s4, s4, 0x1800
	s_and_b32 s5, s5, 0x7e0
	s_or_b32 s46, s4, s5
	s_lshl_b32 s4, s12, 1
	v_and_b32_e32 v15, 0x7f, v14
	s_and_b32 s48, s4, 0x380
	v_or_b32_e32 v2, s48, v15
	v_lshlrev_b32_e32 v82, 2, v2
	v_lshl_add_u64 v[2:3], s[42:43], 0, v[82:83]
	s_mov_b32 s4, 0x21481000
	v_add_co_u32_e32 v10, vcc, s4, v2
	s_lshl_b32 s4, s48, 1
	v_ashrrev_i32_e32 v16, 7, v14
	s_add_u32 s4, s42, s4
	v_lshlrev_b32_e32 v2, 3, v16
	v_lshlrev_b32_e32 v82, 1, v15
	s_addc_u32 s5, s43, 0
	s_mov_b32 s47, s13
	v_addc_co_u32_e32 v11, vcc, 0, v3, vcc
	v_ashrrev_i32_e32 v3, 31, v2
	v_lshl_add_u64 v[6:7], s[4:5], 0, v[82:83]
	s_mov_b64 s[4:5], 0x2d482000
	v_lshl_add_u64 v[4:5], v[2:3], 0, s[46:47]
	v_lshl_add_u64 v[8:9], v[6:7], 0, s[4:5]
	v_mad_i64_i32 v[8:9], s[4:5], v4, s60, v[8:9]
	s_movk_i32 s5, 0x6000
	s_nop 0
	v_add_co_u32_e32 v12, vcc, s5, v8
	s_movk_i32 s4, 0x5000
	s_nop 0
	v_addc_co_u32_e32 v13, vcc, 0, v9, vcc
	global_load_dword v23, v[10:11], off
	global_load_ushort v20, v[12:13], off
	global_load_ushort v21, v[8:9], off offset:2048
	v_add_co_u32_e32 v10, vcc, s4, v8
	s_movk_i32 s4, 0x1000
	s_nop 0
	v_addc_co_u32_e32 v11, vcc, 0, v9, vcc
	s_waitcnt vmcnt(18)
	v_add_co_u32_e32 v18, vcc, s4, v8
	s_mov_b32 s4, 0xb000
	s_nop 0
	v_addc_co_u32_e32 v19, vcc, 0, v9, vcc
	global_load_ushort v17, v[12:13], off offset:2048
	s_nop 0
	global_load_ushort v18, v[18:19], off
	s_nop 0
	global_load_ushort v12, v[8:9], off
	global_load_ushort v13, v[10:11], off offset:2048
	v_add_co_u32_e32 v10, vcc, s4, v8
	v_lshl_add_u64 v[6:7], v[6:7], 0, s[20:21]
	s_nop 0
	v_addc_co_u32_e32 v11, vcc, 0, v9, vcc
	global_load_ushort v36, v[10:11], off offset:2048
	v_lshlrev_b64 v[4:5], 11, v[4:5]
	v_readfirstlane_b32 s49, v14
	s_waitcnt vmcnt(7)
	v_sub_f32_e32 v24, 1.0, v23
	s_waitcnt vmcnt(6)
	v_lshlrev_b32_e32 v11, 16, v20
	s_waitcnt vmcnt(5)
	v_lshlrev_b32_e32 v10, 16, v21
	v_max_f32_e32 v10, v10, v10
	v_med3_f32 v10, v10, s61, v102
	v_mul_f32_e32 v10, 0xbfb8aa3b, v10
	v_exp_f32_e32 v10, v10
	v_max_f32_e32 v11, v11, v11
	v_med3_f32 v11, v11, s61, v102
	v_mul_f32_e32 v11, 0xbfb8aa3b, v11
	v_exp_f32_e32 v37, v11
	v_add_f32_e32 v11, 1.0, v10
	s_waitcnt vmcnt(2)
	v_lshlrev_b32_e32 v20, 16, v12
	v_div_scale_f32 v12, s[4:5], v11, v11, 1.0
	v_rcp_f32_e32 v26, v12
	v_div_scale_f32 v21, s[4:5], v11, v11, v10
	v_rcp_f32_e32 v27, v21
	v_fma_f32 v30, -v12, v26, 1.0
	s_waitcnt vmcnt(1)
	v_lshlrev_b32_e32 v19, 16, v13
	v_div_scale_f32 v13, vcc, 1.0, v11, 1.0
	v_fmac_f32_e32 v26, v30, v26
	v_mul_f32_e32 v30, v13, v26
	v_fma_f32 v31, -v21, v27, 1.0
	v_fma_f32 v33, -v12, v30, v13
	v_div_scale_f32 v22, s[4:5], v10, v11, v10
	v_fmac_f32_e32 v27, v31, v27
	v_fmac_f32_e32 v30, v33, v26
	v_mul_f32_e32 v31, v22, v27
	v_fma_f32 v12, -v12, v30, v13
	v_fma_f32 v34, -v21, v31, v22
	v_div_fmas_f32 v12, v12, v26, v30
	v_fmac_f32_e32 v31, v34, v27
	v_div_fixup_f32 v12, v12, v11, 1.0
	v_fma_f32 v13, -v21, v31, v22
	s_mov_b64 vcc, s[4:5]
	v_fma_f32 v12, v24, v12, v23
	v_div_fmas_f32 v13, v13, v27, v31
	v_cmp_gt_f32_e32 vcc, s62, v12
	v_add_f32_e32 v38, 1.0, v37
	v_div_scale_f32 v25, s[6:7], v38, v38, 1.0
	v_cndmask_b32_e64 v21, 0, 32, vcc
	v_ldexp_f32 v12, v12, v21
	v_log_f32_e32 v12, v12
	v_rcp_f32_e32 v28, v25
	v_div_fixup_f32 v10, v13, v11, v10
	v_div_scale_f32 v29, s[6:7], 1.0, v38, 1.0
	v_mul_f32_e32 v11, 0x3f317217, v12
	v_fma_f32 v11, v12, s63, -v11
	v_fma_f32 v32, -v25, v28, 1.0
	v_fmac_f32_e32 v11, 0x3377d1cf, v12
	v_fmac_f32_e32 v28, v32, v28
	v_mul_f32_e32 v21, v24, v10
	v_cndmask_b32_e32 v10, 0, v103, vcc
	v_fmac_f32_e32 v11, 0x3f317217, v12
	v_cmp_lt_f32_e64 vcc, |v12|, s64
	v_mul_f32_e32 v32, v29, v28
	v_fma_f32 v35, -v25, v32, v29
	v_cndmask_b32_e32 v11, v12, v11, vcc
	v_div_scale_f32 v12, s[4:5], v38, v38, v37
	v_rcp_f32_e32 v39, v12
	v_fmac_f32_e32 v32, v35, v28
	v_sub_f32_e32 v10, v11, v10
	v_add_f32_e32 v22, 0, v10
	v_fma_f32 v10, -v25, v32, v29
	s_mov_b64 vcc, s[6:7]
	v_div_fmas_f32 v10, v10, v28, v32
	v_div_fixup_f32 v13, v10, v38, 1.0
	v_fma_f32 v10, -v12, v39, 1.0
	v_fmac_f32_e32 v39, v10, v39
	v_div_scale_f32 v25, vcc, v37, v38, v37
	s_mov_b32 s4, 0xc000
	v_mul_f32_e32 v40, v25, v39
	v_add_co_u32_e64 v10, s[4:5], s4, v8
	v_fma_f32 v26, -v12, v40, v25
	s_nop 0
	v_addc_co_u32_e64 v11, s[4:5], 0, v9, s[4:5]
	v_fmac_f32_e32 v40, v26, v39
	s_mov_b32 s4, 0x10000
	global_load_ushort v41, v[10:11], off offset:-4096
	v_fma_f32 v42, -v12, v40, v25
	v_add_co_u32_e64 v12, s[4:5], s4, v8
	v_fma_f32 v43, v24, v13, v23
	s_nop 0
	v_addc_co_u32_e64 v13, s[4:5], 0, v9, s[4:5]
	s_mov_b32 s4, 0x11000
	s_nop 0
	v_add_co_u32_e64 v28, s[4:5], s4, v8
	s_waitcnt vmcnt(0)
; __device__ __forceinline__ float bf2f(bf16 b) { return __uint_as_float(((unsigned)b) << 16); }
; __device__ __forceinline__ void hgrn_x1_unit(const Args& a, int layer, int unit, LAS unsigned char* lds) {
;     ...
;     for (int i = 0; i < 8; ++i) {
;         const bf16* pr = PROJ + (tok0 + 8 * tq + i) * DIN + h * 128 + d;
;         q[i] = bf2f(pr[C_QA]); vv[i] = pr[C_IA];
;         float z = bf2f(pr[C_FA]); z = fminf(fmaxf(z, -30.f), 30.f);
;         const float e = __expf(-z), sp = 1.0f / (1.0f + e), sn = e / (1.0f + e);
;         const float f = lb + (1.0f - lb) * sp; kk[i] = (1.0f - lb) * sn;
;         run += __logf(f); c[i] = run;
;     }
	v_lshlrev_b32_e32 v54, 16, v41
	v_addc_co_u32_e64 v29, s[4:5], 0, v9, s[4:5]
	s_mov_b32 s4, 0x16000
	s_nop 0
	v_add_co_u32_e64 v26, s[4:5], s4, v8
	s_nop 1
	v_addc_co_u32_e64 v27, s[4:5], 0, v9, s[4:5]
	v_add_co_u32_e64 v30, s[4:5], s67, v8
	s_nop 1
	v_addc_co_u32_e64 v31, s[4:5], 0, v9, s[4:5]
	v_add_co_u32_e64 v32, s[4:5], s68, v8
	s_nop 1
	v_addc_co_u32_e64 v33, s[4:5], 0, v9, s[4:5]
	v_add_co_u32_e64 v34, s[4:5], s69, v8
	s_nop 1
	v_addc_co_u32_e64 v35, s[4:5], 0, v9, s[4:5]
	global_load_ushort v44, v[12:13], off offset:2048
	global_load_ushort v25, v[28:29], off offset:2048
	global_load_ushort v45, v[26:27], off offset:2048
	global_load_ushort v46, v[30:31], off offset:2048
	s_nop 0
	global_load_ushort v26, v[32:33], off offset:2048
	s_nop 0
	global_load_ushort v34, v[34:35], off offset:2048
	s_nop 0
	global_load_ushort v32, v[32:33], off
	s_nop 0
	global_load_ushort v33, v[28:29], off
	v_cmp_gt_f32_e64 s[4:5], s62, v43
	v_div_fmas_f32 v13, v42, v39, v40
	v_div_fixup_f32 v13, v13, v38, v37
	v_cndmask_b32_e64 v12, 0, 32, s[4:5]
	v_ldexp_f32 v12, v43, v12
	v_log_f32_e32 v12, v12
	v_mul_f32_e32 v52, v24, v13
	v_mul_f32_e32 v13, 0x3f317217, v12
	v_fma_f32 v13, v12, s63, -v13
	v_fmac_f32_e32 v13, 0x3377d1cf, v12
	v_fmac_f32_e32 v13, 0x3f317217, v12
	v_cmp_lt_f32_e64 vcc, |v12|, s64
	s_waitcnt vmcnt(7)
	v_lshlrev_b32_e32 v57, 16, v44
	v_cndmask_b32_e32 v12, v12, v13, vcc
	v_lshlrev_b32_e32 v13, 16, v36
	v_max_f32_e32 v13, v13, v13
	v_med3_f32 v13, v13, s61, v102
	v_mul_f32_e32 v13, 0xbfb8aa3b, v13
	v_exp_f32_e32 v35, v13
	v_cndmask_b32_e64 v13, 0, v103, s[4:5]
	v_add_co_u32_e32 v28, vcc, s66, v8
	v_sub_f32_e32 v12, v12, v13
	s_nop 0
	v_addc_co_u32_e32 v29, vcc, 0, v9, vcc
	v_add_f32_e32 v53, v22, v12
	v_add_co_u32_e32 v12, vcc, s70, v8
	v_add_f32_e32 v36, 1.0, v35
	s_nop 0
	v_addc_co_u32_e32 v13, vcc, 0, v9, vcc
	v_add_co_u32_e32 v30, vcc, s72, v8
	v_div_scale_f32 v37, s[4:5], v36, v36, 1.0
	s_nop 0
	v_addc_co_u32_e32 v31, vcc, 0, v9, vcc
	global_load_ushort v10, v[10:11], off
	s_nop 0
	global_load_ushort v39, v[28:29], off offset:-4096
	global_load_ushort v11, v[28:29], off
	s_nop 0
	global_load_ushort v28, v[12:13], off offset:-4096
	global_load_ushort v27, v[30:31], off offset:2048
	v_rcp_f32_e32 v38, v37
	s_waitcnt vmcnt(5)
	v_lshlrev_b32_e32 v33, 16, v33
	v_max_f32_e32 v33, v33, v33
	v_med3_f32 v33, v33, s61, v102
	v_fma_f32 v29, -v37, v38, 1.0
	v_fmac_f32_e32 v38, v29, v38
	v_div_scale_f32 v29, vcc, 1.0, v36, 1.0
	v_mul_f32_e32 v40, v29, v38
	v_fma_f32 v41, -v37, v40, v29
	v_fmac_f32_e32 v40, v41, v38
	v_fma_f32 v29, -v37, v40, v29
	v_div_scale_f32 v37, s[4:5], v36, v36, v35
	v_rcp_f32_e32 v41, v37
	v_div_fmas_f32 v29, v29, v38, v40
	v_div_fixup_f32 v29, v29, v36, 1.0
	v_fma_f32 v29, v24, v29, v23
	v_fma_f32 v38, -v37, v41, 1.0
	v_fmac_f32_e32 v41, v38, v41
	v_div_scale_f32 v38, vcc, v35, v36, v35
	v_mul_f32_e32 v40, v38, v41
	v_fma_f32 v42, -v37, v40, v38
	v_fmac_f32_e32 v40, v42, v41
	v_cmp_gt_f32_e64 s[4:5], s62, v29
	v_fma_f32 v37, -v37, v40, v38
	v_div_fmas_f32 v37, v37, v41, v40
	v_cndmask_b32_e64 v38, 0, 32, s[4:5]
	v_ldexp_f32 v29, v29, v38
	v_log_f32_e32 v29, v29
	v_mul_f32_e32 v33, 0xbfb8aa3b, v33
	v_div_fixup_f32 v35, v37, v36, v35
	v_exp_f32_e32 v33, v33
	v_mul_f32_e32 v55, v24, v35
	v_mul_f32_e32 v35, 0x3f317217, v29
	v_fma_f32 v35, v29, s63, -v35
	v_fmac_f32_e32 v35, 0x3377d1cf, v29
	v_fmac_f32_e32 v35, 0x3f317217, v29
	v_cmp_lt_f32_e64 vcc, |v29|, s64
	v_add_f32_e32 v36, 1.0, v33
	v_lshlrev_b32_e32 v32, 16, v32
	v_cndmask_b32_e32 v29, v29, v35, vcc
	v_cndmask_b32_e64 v35, 0, v103, s[4:5]
	v_div_scale_f32 v37, s[4:5], v36, v36, 1.0
	v_rcp_f32_e32 v38, v37
	v_sub_f32_e32 v29, v29, v35
	v_add_f32_e32 v56, v53, v29
	v_max_f32_e32 v32, v32, v32
	v_fma_f32 v29, -v37, v38, 1.0
	v_fmac_f32_e32 v38, v29, v38
	v_div_scale_f32 v29, vcc, 1.0, v36, 1.0
	v_mul_f32_e32 v35, v29, v38
	v_fma_f32 v40, -v37, v35, v29
	v_fmac_f32_e32 v35, v40, v38
	v_fma_f32 v29, -v37, v35, v29
	v_div_scale_f32 v37, s[4:5], v36, v36, v33
	v_rcp_f32_e32 v40, v37
	v_div_fmas_f32 v29, v29, v38, v35
	v_div_fixup_f32 v29, v29, v36, 1.0
	v_fma_f32 v29, v24, v29, v23
	v_fma_f32 v35, -v37, v40, 1.0
	v_fmac_f32_e32 v40, v35, v40
	v_div_scale_f32 v35, vcc, v33, v36, v33
	v_mul_f32_e32 v38, v35, v40
	v_fma_f32 v41, -v37, v38, v35
	v_fmac_f32_e32 v38, v41, v40
	v_fma_f32 v35, -v37, v38, v35
	v_cmp_gt_f32_e64 s[4:5], s62, v29
	v_div_fmas_f32 v35, v35, v40, v38
	v_div_fixup_f32 v33, v35, v36, v33
	v_cndmask_b32_e64 v37, 0, 32, s[4:5]
	v_ldexp_f32 v29, v29, v37
	v_lshlrev_b32_e32 v35, 16, v45
	v_log_f32_e32 v29, v29
	v_max_f32_e32 v35, v35, v35
	v_med3_f32 v35, v35, s61, v102
	v_mul_f32_e32 v35, 0xbfb8aa3b, v35
	v_exp_f32_e32 v35, v35
	v_mul_f32_e32 v58, v24, v33
	v_mul_f32_e32 v33, 0x3f317217, v29
	v_fma_f32 v33, v29, s63, -v33
	v_fmac_f32_e32 v33, 0x3377d1cf, v29
	v_fmac_f32_e32 v33, 0x3f317217, v29
	v_cmp_lt_f32_e64 vcc, |v29|, s64
	v_add_f32_e32 v36, 1.0, v35
	s_waitcnt vmcnt(3)
; __device__ __forceinline__ float bf2f(bf16 b) { return __uint_as_float(((unsigned)b) << 16); }
; __device__ __forceinline__ void hgrn_x1_unit(const Args& a, int layer, int unit, LAS unsigned char* lds) {
;     ...
;     for (int i = 0; i < 8; ++i) {
;         const bf16* pr = PROJ + (tok0 + 8 * tq + i) * DIN + h * 128 + d;
;         q[i] = bf2f(pr[C_QA]); vv[i] = pr[C_IA];
;         float z = bf2f(pr[C_FA]); z = fminf(fmaxf(z, -30.f), 30.f);
;         const float e = __expf(-z), sp = 1.0f / (1.0f + e), sn = e / (1.0f + e);
;         const float f = lb + (1.0f - lb) * sp; kk[i] = (1.0f - lb) * sn;
;         run += __logf(f); c[i] = run;
;     }
;     __syncthreads();
;     TOT[tq * 128 + d] = run;
;     __syncthreads();
	v_lshlrev_b32_e32 v60, 16, v39
	v_cndmask_b32_e32 v29, v29, v33, vcc
	v_cndmask_b32_e64 v33, 0, v103, s[4:5]
	v_div_scale_f32 v37, s[4:5], v36, v36, 1.0
	v_rcp_f32_e32 v38, v37
	v_sub_f32_e32 v29, v29, v33
	v_add_f32_e32 v59, v56, v29
	v_med3_f32 v32, v32, s61, v102
	v_fma_f32 v29, -v37, v38, 1.0
	v_fmac_f32_e32 v38, v29, v38
	v_div_scale_f32 v29, vcc, 1.0, v36, 1.0
	v_mul_f32_e32 v33, v29, v38
	v_fma_f32 v39, -v37, v33, v29
	v_fmac_f32_e32 v33, v39, v38
	v_fma_f32 v29, -v37, v33, v29
	v_div_scale_f32 v37, s[4:5], v36, v36, v35
	v_rcp_f32_e32 v39, v37
	v_div_fmas_f32 v29, v29, v38, v33
	v_div_fixup_f32 v29, v29, v36, 1.0
	v_fma_f32 v29, v24, v29, v23
	v_fma_f32 v33, -v37, v39, 1.0
	v_fmac_f32_e32 v39, v33, v39
	v_div_scale_f32 v33, vcc, v35, v36, v35
	v_mul_f32_e32 v38, v33, v39
	v_fma_f32 v40, -v37, v38, v33
	v_fmac_f32_e32 v38, v40, v39
	v_cmp_gt_f32_e64 s[4:5], s62, v29
	v_fma_f32 v33, -v37, v38, v33
	v_div_fmas_f32 v33, v33, v39, v38
	v_cndmask_b32_e64 v37, 0, 32, s[4:5]
	v_ldexp_f32 v29, v29, v37
	v_log_f32_e32 v29, v29
	v_mul_f32_e32 v32, 0xbfb8aa3b, v32
	v_div_fixup_f32 v33, v33, v36, v35
	v_exp_f32_e32 v32, v32
	v_mul_f32_e32 v61, v24, v33
	v_mul_f32_e32 v33, 0x3f317217, v29
	v_fma_f32 v33, v29, s63, -v33
	v_fmac_f32_e32 v33, 0x3377d1cf, v29
	v_fmac_f32_e32 v33, 0x3f317217, v29
	v_cmp_lt_f32_e64 vcc, |v29|, s64
	v_add_f32_e32 v35, 1.0, v32
	s_waitcnt vmcnt(1)
	v_lshlrev_b32_e32 v66, 16, v28
	v_cndmask_b32_e32 v29, v29, v33, vcc
	v_cndmask_b32_e64 v33, 0, v103, s[4:5]
	v_div_scale_f32 v36, s[4:5], v35, v35, 1.0
	v_add_co_u32_e64 v8, s[4:5], s71, v8
	v_rcp_f32_e32 v37, v36
	s_nop 0
	v_addc_co_u32_e64 v9, s[4:5], 0, v9, s[4:5]
	global_load_ushort v8, v[8:9], off offset:2048
	s_nop 0
	global_load_ushort v9, v[30:31], off
	v_sub_f32_e32 v29, v29, v33
	v_add_f32_e32 v62, v59, v29
	v_fma_f32 v29, -v36, v37, 1.0
	v_fmac_f32_e32 v37, v29, v37
	v_div_scale_f32 v29, vcc, 1.0, v35, 1.0
	v_div_scale_f32 v30, s[4:5], v35, v35, v32
	v_mul_f32_e32 v33, v29, v37
	v_rcp_f32_e32 v31, v30
	v_fma_f32 v38, -v36, v33, v29
	v_fmac_f32_e32 v33, v38, v37
	v_fma_f32 v29, -v36, v33, v29
	v_div_fmas_f32 v29, v29, v37, v33
	v_fma_f32 v33, -v30, v31, 1.0
	v_fmac_f32_e32 v31, v33, v31
	v_div_scale_f32 v33, vcc, v32, v35, v32
	v_div_fixup_f32 v29, v29, v35, 1.0
	v_mul_f32_e32 v36, v33, v31
	v_fma_f32 v37, -v30, v36, v33
	v_fma_f32 v29, v24, v29, v23
	v_fmac_f32_e32 v36, v37, v31
	v_cmp_gt_f32_e64 s[4:5], s62, v29
	v_fma_f32 v30, -v30, v36, v33
	v_div_fmas_f32 v30, v30, v31, v36
	v_cndmask_b32_e64 v33, 0, 32, s[4:5]
	v_ldexp_f32 v29, v29, v33
	v_log_f32_e32 v29, v29
	v_lshlrev_b32_e32 v31, 16, v34
	v_max_f32_e32 v31, v31, v31
	v_div_fixup_f32 v30, v30, v35, v32
	v_med3_f32 v31, v31, s61, v102
	v_mul_f32_e32 v64, v24, v30
	v_mul_f32_e32 v30, 0x3f317217, v29
	v_mul_f32_e32 v31, 0xbfb8aa3b, v31
	v_fma_f32 v30, v29, s63, -v30
	v_exp_f32_e32 v31, v31
	v_fmac_f32_e32 v30, 0x3377d1cf, v29
	v_fmac_f32_e32 v30, 0x3f317217, v29
	v_cmp_lt_f32_e64 vcc, |v29|, s64
	global_load_ushort v67, v[12:13], off
	s_nop 0
	v_cndmask_b32_e32 v29, v29, v30, vcc
	v_cndmask_b32_e64 v30, 0, v103, s[4:5]
	v_sub_f32_e32 v29, v29, v30
	v_add_f32_e32 v30, 1.0, v31
	v_div_scale_f32 v32, s[4:5], v30, v30, 1.0
	v_rcp_f32_e32 v33, v32
	v_add_f32_e32 v65, v62, v29
	s_barrier
	v_fma_f32 v12, -v32, v33, 1.0
	v_fmac_f32_e32 v33, v12, v33
	v_div_scale_f32 v12, vcc, 1.0, v30, 1.0
	v_mul_f32_e32 v13, v12, v33
	v_fma_f32 v28, -v32, v13, v12
	v_fmac_f32_e32 v13, v28, v33
	v_div_scale_f32 v28, s[4:5], v30, v30, v31
	v_rcp_f32_e32 v29, v28
	v_fma_f32 v12, -v32, v13, v12
	v_div_fmas_f32 v12, v12, v33, v13
	v_div_fixup_f32 v12, v12, v30, 1.0
	v_fma_f32 v13, -v28, v29, 1.0
	v_fmac_f32_e32 v29, v13, v29
	v_div_scale_f32 v13, vcc, v31, v30, v31
	v_mul_f32_e32 v32, v13, v29
	v_fma_f32 v33, -v28, v32, v13
	v_fma_f32 v12, v24, v12, v23
	v_fmac_f32_e32 v32, v33, v29
	v_cmp_gt_f32_e64 s[4:5], s62, v12
	v_fma_f32 v13, -v28, v32, v13
	v_div_fmas_f32 v13, v13, v29, v32
	v_cndmask_b32_e64 v28, 0, 32, s[4:5]
	v_ldexp_f32 v12, v12, v28
	s_waitcnt vmcnt(1)
	v_lshlrev_b32_e32 v9, 16, v9
	v_log_f32_e32 v12, v12
	v_max_f32_e32 v9, v9, v9
	v_med3_f32 v9, v9, s61, v102
	v_mul_f32_e32 v9, 0xbfb8aa3b, v9
	v_div_fixup_f32 v13, v13, v30, v31
	v_exp_f32_e32 v9, v9
	v_mul_f32_e32 v68, v24, v13
	v_mul_f32_e32 v13, 0x3f317217, v12
	v_fma_f32 v13, v12, s63, -v13
	v_fmac_f32_e32 v13, 0x3377d1cf, v12
	v_fmac_f32_e32 v13, 0x3f317217, v12
	v_cmp_lt_f32_e64 vcc, |v12|, s64
	v_add_f32_e32 v28, 1.0, v9
	v_lshlrev_b32_e32 v70, 16, v8
	v_cndmask_b32_e32 v12, v12, v13, vcc
	v_cndmask_b32_e64 v13, 0, v103, s[4:5]
	v_div_scale_f32 v29, s[4:5], v28, v28, 1.0
	v_rcp_f32_e32 v30, v29
	v_sub_f32_e32 v12, v12, v13
	v_add_f32_e32 v69, v65, v12
	v_lshl_add_u64 v[36:37], v[6:7], 0, v[4:5]
	v_fma_f32 v8, -v29, v30, 1.0
	v_fmac_f32_e32 v30, v8, v30
	v_div_scale_f32 v8, vcc, 1.0, v28, 1.0
	v_mul_f32_e32 v12, v8, v30
	v_fma_f32 v13, -v29, v12, v8
	v_fmac_f32_e32 v12, v13, v30
	v_div_scale_f32 v13, s[4:5], v28, v28, v9
	v_fma_f32 v8, -v29, v12, v8
	v_rcp_f32_e32 v29, v13
	v_div_fmas_f32 v8, v8, v30, v12
	v_div_fixup_f32 v8, v8, v28, 1.0
	v_fmac_f32_e32 v23, v24, v8
	v_fma_f32 v12, -v13, v29, 1.0
	v_cmp_gt_f32_e64 s[4:5], s62, v23
	v_fmac_f32_e32 v29, v12, v29
	v_div_scale_f32 v12, vcc, v9, v28, v9
	v_cndmask_b32_e64 v8, 0, 32, s[4:5]
	v_mul_f32_e32 v30, v12, v29
	v_ldexp_f32 v8, v23, v8
	v_fma_f32 v31, -v13, v30, v12
	v_log_f32_e32 v8, v8
	v_fmac_f32_e32 v30, v31, v29
	v_fma_f32 v12, -v13, v30, v12
	v_div_fmas_f32 v12, v12, v29, v30
	v_div_fixup_f32 v23, v12, v28, v9
	v_mul_f32_e32 v9, 0x3f317217, v8
	v_fma_f32 v9, v8, s63, -v9
	v_fmac_f32_e32 v9, 0x3377d1cf, v8
	v_fmac_f32_e32 v9, 0x3f317217, v8
	v_cmp_lt_f32_e64 vcc, |v8|, s64
	v_or_b32_e32 v4, 1, v2
	v_ashrrev_i32_e32 v5, 31, v4
	v_cndmask_b32_e32 v8, v8, v9, vcc
	v_cndmask_b32_e64 v9, 0, v103, s[4:5]
	v_sub_f32_e32 v8, v8, v9
	v_add_f32_e32 v9, v69, v8
	v_lshl_add_u32 v8, v14, 2, 0
	ds_write_b32 v8, v9
	v_lshl_add_u32 v8, v15, 2, 0
	s_waitcnt lgkmcnt(0)
	s_barrier
; #define LAS __attribute__((address_space(3)))
; __device__ __forceinline__ bf16 f2bf(float f) { return (bf16)(pk2(f, 0.f) & 0xffffu); }
; __device__ __forceinline__ void hgrn_x1_unit(const Args& a, int layer, int unit, LAS unsigned char* lds) {
;     ...
;     float off = 0.f, bl = 0.f;
; #pragma unroll
;     for (int g = 0; g < 4; ++g) { const float t = TOT[g * 128 + d]; bl += t; off += (g < tq) ? t : 0.f; }
;     unsigned kh[8];
; #pragma unroll
;     for (int i = 0; i < 8; ++i) {
;         const float bt = off + c[i];
;         const float qt = q[i] * __expf(bt), kh_ = kk[i] * __expf(bl - bt), kp = kk[i] * __expf(fminf(-bt, 80.f));
;         const int t = 8 * tq + i;
;         const bf16 qb = f2bf(qt);
;         *(LAS bf16*)(lds + HX_QL + t * 272 + d * 2) = qb;
;         *(LAS bf16*)(lds + HX_KP + t * 272 + d * 2) = f2bf(kp);
;         QT[(tok0 + t) * 1024 + h * 128 + d] = qb;
;         kh[i] = f2bf(kh_);
;     }
;     { u32x4 o; o.x = kh[0] | (kh[1] << 16); o.y = kh[2] | (kh[3] << 16); o.z = kh[4] | (kh[5] << 16); o.w = kh[6] | (kh[7] << 16); *(u32x4*)(KT + d * 32 + 8 * tq) = o;
	ds_read2st64_b32 v[12:13], v8 offset1:2
	ds_read2st64_b32 v[28:29], v8 offset0:4 offset1:6
	v_sub_u32_e32 v8, v8, v82
	v_mad_u64_u32 v[38:39], s[6:7], v4, s74, v[8:9]
	v_lshl_add_u64 v[4:5], v[4:5], 0, s[46:47]
	v_lshlrev_b64 v[4:5], 11, v[4:5]
	v_lshl_add_u64 v[40:41], v[6:7], 0, v[4:5]
	v_or_b32_e32 v4, 2, v2
	v_ashrrev_i32_e32 v5, 31, v4
	v_lshl_add_u64 v[4:5], v[4:5], 0, s[46:47]
	v_lshlrev_b64 v[4:5], 11, v[4:5]
	v_lshl_add_u64 v[42:43], v[6:7], 0, v[4:5]
	v_or_b32_e32 v4, 3, v2
	v_ashrrev_i32_e32 v5, 31, v4
	v_lshl_add_u64 v[4:5], v[4:5], 0, s[46:47]
	v_lshlrev_b64 v[4:5], 11, v[4:5]
	v_lshl_add_u64 v[44:45], v[6:7], 0, v[4:5]
	v_or_b32_e32 v4, 4, v2
	v_ashrrev_i32_e32 v5, 31, v4
	v_lshl_add_u64 v[4:5], v[4:5], 0, s[46:47]
	v_lshlrev_b64 v[4:5], 11, v[4:5]
	v_lshlrev_b32_e32 v63, 16, v46
	v_lshl_add_u64 v[46:47], v[6:7], 0, v[4:5]
	v_or_b32_e32 v4, 5, v2
	v_ashrrev_i32_e32 v5, 31, v4
	v_lshl_add_u64 v[4:5], v[4:5], 0, s[46:47]
	v_lshlrev_b64 v[4:5], 11, v[4:5]
	v_cmp_lt_i32_e32 vcc, 1, v16
	v_lshl_add_u64 v[48:49], v[6:7], 0, v[4:5]
	v_or_b32_e32 v4, 6, v2
	v_mul_f32_e32 v23, v24, v23
	s_waitcnt lgkmcnt(1)
	v_cndmask_b32_e32 v24, 0, v13, vcc
	v_cmp_lt_i32_e32 vcc, 2, v16
	v_ashrrev_i32_e32 v5, 31, v4
	v_lshl_add_u64 v[4:5], v[4:5], 0, s[46:47]
	s_waitcnt lgkmcnt(0)
	v_cndmask_b32_e32 v31, 0, v28, vcc
	v_cmp_lt_i32_e32 vcc, 3, v16
	v_lshlrev_b64 v[50:51], 11, v[4:5]
	v_add_f32_e32 v4, 0, v12
	v_cndmask_b32_e32 v33, 0, v29, vcc
	v_cmp_lt_i32_e32 vcc, 0, v16
	v_mov_b32_e32 v30, v13
	v_mov_b32_e32 v32, v28
	v_cndmask_b32_e32 v5, 0, v4, vcc
	v_add_f32_e32 v5, v5, v24
	v_pk_add_f32 v[4:5], v[4:5], v[30:31]
	v_mad_u64_u32 v[34:35], s[6:7], v16, s73, v[8:9]
	v_pk_add_f32 v[12:13], v[4:5], v[32:33]
	v_mov_b32_e32 v8, v29
	v_add_f32_e32 v22, v22, v13
	v_mul_f32_e32 v4, 0x3fb8aa3b, v22
	v_exp_f32_e32 v24, v4
	v_pk_add_f32 v[4:5], v[12:13], v[8:9]
	s_lshl_b64 s[4:5], s[12:13], 13
	v_sub_f32_e32 v8, v4, v22
	v_mul_f32_e32 v8, 0x3fb8aa3b, v8
	v_exp_f32_e32 v12, v8
	v_min_f32_e64 v8, -v22, s76
	v_mul_f32_e32 v8, 0x3fb8aa3b, v8
	v_exp_f32_e32 v22, v8
	v_mul_f32_e32 v20, v24, v20
	v_mul_f32_e32 v12, v21, v12
	v_cvt_pk_bf16_f32 v20, v20, v83
	v_mul_f32_e32 v21, v21, v22
	ds_write_b16 v34, v20 offset:2048
	v_cvt_pk_bf16_f32 v21, v21, v83
	v_and_b32_e32 v250, 0x7f, v0
	v_lshrrev_b32_e32 v251, 7, v0
	v_lshrrev_b32_e32 v252, 1, v251
	v_lshlrev_b32_e32 v252, 12, v252
	v_and_b32_e32 v251, 1, v251
	v_lshl_or_b32 v252, v251, 7, v252
	v_lshrrev_b32_e32 v251, 5, v250
	v_lshl_or_b32 v252, v251, 10, v252
	v_bfe_u32 v251, v250, 2, 2
	v_lshl_or_b32 v252, v251, 8, v252
	v_bfe_u32 v251, v250, 4, 1
	v_lshl_or_b32 v252, v251, 3, v252
	v_and_b32_e32 v251, 3, v250
	v_lshl_or_b32 v252, v251, 1, v252
	s_mul_i32 s100, s12, 0x2000
	v_add_u32_e32 v252, s100, v252
	v_add_u32_e32 v252, 0x45c82000, v252
	v_mov_b32_e32 v253, 0
	v_lshl_add_u64 v[252:253], s[42:43], 0, v[252:253]
	global_store_short v[252:253], v20, off
	v_add_f32_e32 v20, v53, v13
	ds_write_b16 v34, v21 offset:10752
	v_mul_f32_e32 v21, 0x3fb8aa3b, v20
	v_sub_f32_e32 v22, v4, v20
	v_min_f32_e64 v20, -v20, s76
	v_exp_f32_e32 v21, v21
	v_mul_f32_e32 v20, 0x3fb8aa3b, v20
	v_exp_f32_e32 v20, v20
	v_mul_f32_e32 v22, 0x3fb8aa3b, v22
	v_exp_f32_e32 v22, v22
	v_mul_f32_e32 v19, v21, v19
	v_cvt_pk_bf16_f32 v12, v12, v83
	v_mul_f32_e32 v20, v52, v20
	v_cvt_pk_bf16_f32 v19, v19, v83
	ds_write_b16 v38, v19 offset:2048
	v_cvt_pk_bf16_f32 v20, v20, v83
	global_store_short v[252:253], v19, off offset:16
	v_add_f32_e32 v19, v56, v13
	v_mul_f32_e32 v21, v52, v22
	ds_write_b16 v38, v20 offset:10752
	v_mul_f32_e32 v20, 0x3fb8aa3b, v19
	v_sub_f32_e32 v22, v4, v19
	v_min_f32_e64 v19, -v19, s76
	v_exp_f32_e32 v20, v20
	v_mul_f32_e32 v19, 0x3fb8aa3b, v19
	v_mul_f32_e32 v22, 0x3fb8aa3b, v22
	v_exp_f32_e32 v19, v19
	v_exp_f32_e32 v22, v22
	v_mul_f32_e32 v20, v20, v54
	v_cvt_pk_bf16_f32 v21, v21, v83
	v_mul_f32_e32 v19, v55, v19
	v_cvt_pk_bf16_f32 v20, v20, v83
	v_mul_f32_e32 v22, v55, v22
	ds_write_b16 v38, v20 offset:2320
	v_cvt_pk_bf16_f32 v19, v19, v83
	global_store_short v[252:253], v20, off offset:32
	v_add_f32_e32 v20, v59, v13
	ds_write_b16 v38, v19 offset:11024
	v_cvt_pk_bf16_f32 v19, v22, v83
	v_mul_f32_e32 v22, 0x3fb8aa3b, v20
	v_sub_f32_e32 v24, v4, v20
	v_min_f32_e64 v20, -v20, s76
; #define LAS __attribute__((address_space(3)))
; __device__ __forceinline__ bf16 f2bf(float f) { return (bf16)(pk2(f, 0.f) & 0xffffu); }
; __device__ __forceinline__ void hgrn_x1_unit(const Args& a, int layer, int unit, LAS unsigned char* lds) {
;     ...
;     for (int i = 0; i < 8; ++i) {
;         const float bt = off + c[i];
;         const float qt = q[i] * __expf(bt), kh_ = kk[i] * __expf(bl - bt), kp = kk[i] * __expf(fminf(-bt, 80.f));
;         const int t = 8 * tq + i;
;         const bf16 qb = f2bf(qt);
;         *(LAS bf16*)(lds + HX_QL + t * 272 + d * 2) = qb;
;         *(LAS bf16*)(lds + HX_KP + t * 272 + d * 2) = f2bf(kp);
;         QT[(tok0 + t) * 1024 + h * 128 + d] = qb;
;         kh[i] = f2bf(kh_);
;     }
;     { u32x4 o; o.x = kh[0] | (kh[1] << 16); o.y = kh[2] | (kh[3] << 16); o.z = kh[4] | (kh[5] << 16); o.w = kh[6] | (kh[7] << 16); *(u32x4*)(KT + d * 32 + 8 * tq) = o;
;       u32x4 w; w.x = vv[0] | ((unsigned)vv[1] << 16); w.y = vv[2] | ((unsigned)vv[3] << 16); w.z = vv[4] | ((unsigned)vv[5] << 16); w.w = vv[6] | ((unsigned)vv[7] << 16);
;       *(u32x4*)(VT + d * 32 + 8 * tq) = w; *(LAS u32x4*)(lds + HX_VL + d * 80 + 16 * tq) = w; }
;     if (tq == 0) DEC[d] = __expf(bl);
	v_mul_f32_e32 v20, 0x3fb8aa3b, v20
	v_exp_f32_e32 v22, v22
	v_exp_f32_e32 v20, v20
	v_mul_f32_e32 v24, 0x3fb8aa3b, v24
	v_exp_f32_e32 v24, v24
	v_mul_f32_e32 v22, v22, v57
	v_mul_f32_e32 v20, v58, v20
	v_cvt_pk_bf16_f32 v22, v22, v83
	ds_write_b16 v38, v22 offset:2592
	v_cvt_pk_bf16_f32 v20, v20, v83
	ds_write_b16 v38, v20 offset:11296
	v_add_f32_e32 v20, v62, v13
	global_store_short v[252:253], v22, off offset:48
	v_mul_f32_e32 v22, 0x3fb8aa3b, v20
	v_sub_f32_e32 v28, v4, v20
	v_min_f32_e64 v20, -v20, s76
	v_exp_f32_e32 v22, v22
	v_mul_f32_e32 v20, 0x3fb8aa3b, v20
	v_mul_f32_e32 v28, 0x3fb8aa3b, v28
	v_exp_f32_e32 v20, v20
	v_exp_f32_e32 v28, v28
	v_mul_f32_e32 v24, v58, v24
	v_mul_f32_e32 v22, v22, v60
	v_cvt_pk_bf16_f32 v24, v24, v83
	v_mul_f32_e32 v20, v61, v20
	v_cvt_pk_bf16_f32 v22, v22, v83
	v_mul_f32_e32 v28, v61, v28
	ds_write_b16 v38, v22 offset:2864
	v_cvt_pk_bf16_f32 v20, v20, v83
	global_store_short v[252:253], v22, off offset:64
	v_add_f32_e32 v22, v65, v13
	ds_write_b16 v38, v20 offset:11568
	v_cvt_pk_bf16_f32 v20, v28, v83
	v_mul_f32_e32 v28, 0x3fb8aa3b, v22
	v_sub_f32_e32 v29, v4, v22
	v_min_f32_e64 v22, -v22, s76
	v_mul_f32_e32 v22, 0x3fb8aa3b, v22
	v_exp_f32_e32 v28, v28
	v_exp_f32_e32 v22, v22
	v_add_f32_e32 v13, v69, v13
	v_mul_f32_e32 v29, 0x3fb8aa3b, v29
	v_mul_f32_e32 v28, v28, v63
	v_mul_f32_e32 v22, v64, v22
	v_cvt_pk_bf16_f32 v28, v28, v83
	ds_write_b16 v38, v28 offset:3136
	v_cvt_pk_bf16_f32 v22, v22, v83
	ds_write_b16 v38, v22 offset:11840
	global_store_short v[252:253], v28, off offset:80
	v_mul_f32_e32 v22, 0x3fb8aa3b, v13
	v_sub_f32_e32 v28, v4, v13
	v_min_f32_e64 v13, -v13, s76
	v_mul_f32_e32 v13, 0x3fb8aa3b, v13
	v_exp_f32_e32 v29, v29
	v_exp_f32_e32 v22, v22
	v_exp_f32_e32 v13, v13
	v_lshl_add_u64 v[8:9], v[6:7], 0, v[50:51]
	v_mul_f32_e32 v29, v64, v29
	v_mul_f32_e32 v22, v22, v66
	v_mul_f32_e32 v13, v68, v13
	v_mul_f32_e32 v28, 0x3fb8aa3b, v28
	v_cvt_pk_bf16_f32 v29, v29, v83
	v_cvt_pk_bf16_f32 v22, v22, v83
	ds_write_b16 v38, v22 offset:3408
	v_cvt_pk_bf16_f32 v13, v13, v83
	v_exp_f32_e32 v28, v28
	ds_write_b16 v38, v13 offset:12112
	global_store_short v[252:253], v22, off offset:96
	v_mul_f32_e32 v9, 0x3fb8aa3b, v5
	v_sub_f32_e32 v13, v4, v5
	v_min_f32_e64 v5, -v5, s76
	v_exp_f32_e32 v9, v9
	v_mul_f32_e32 v13, 0x3fb8aa3b, v13
	v_mul_f32_e32 v5, 0x3fb8aa3b, v5
	v_exp_f32_e32 v13, v13
	v_exp_f32_e32 v5, v5
	v_mul_f32_e32 v28, v68, v28
	v_cvt_pk_bf16_f32 v8, v28, v83
	v_mul_f32_e32 v9, v9, v70
	v_and_b32_e32 v22, 0xffff, v8
	v_or_b32_e32 v8, 7, v2
	v_mul_f32_e32 v13, v23, v13
	v_mul_f32_e32 v5, v23, v5
	v_cvt_pk_bf16_f32 v23, v9, v83
	v_ashrrev_i32_e32 v9, 31, v8
	v_lshl_add_u64 v[8:9], v[8:9], 0, s[46:47]
	s_add_u32 s4, s42, s4
	v_lshlrev_b64 v[8:9], 11, v[8:9]
	s_addc_u32 s5, s43, s5
	v_and_b32_e32 v19, 0xffff, v19
	v_lshl_add_u64 v[6:7], v[6:7], 0, v[8:9]
	v_lshlrev_b32_e32 v82, 6, v15
	ds_write_b16 v38, v23 offset:3680
	v_cvt_pk_bf16_f32 v5, v5, v83
	global_store_short v[252:253], v23, off offset:112
	v_perm_b32 v8, v26, v11, s77
	v_perm_b32 v6, v17, v18, s77
	v_lshl_or_b32 v11, v24, 16, v19
	v_lshl_add_u64 v[18:19], s[4:5], 0, v[82:83]
	v_lshl_add_u64 v[2:3], v[2:3], 1, v[18:19]
	v_add_co_u32_e32 v18, vcc, s78, v2
	s_waitcnt vmcnt(8)
	v_perm_b32 v9, v27, v67, s77
	v_addc_co_u32_e32 v19, vcc, 0, v3, vcc
	v_add_co_u32_e32 v2, vcc, 0x47c82000, v2
	v_perm_b32 v7, v25, v10, s77
	s_nop 0
	v_addc_co_u32_e32 v3, vcc, 0, v3, vcc
	v_and_b32_e32 v12, 0xffff, v12
	v_and_b32_e32 v20, 0xffff, v20
	ds_write_b16 v38, v5 offset:12384
	v_cvt_pk_bf16_f32 v5, v13, v83
	global_store_dwordx4 v[2:3], v[6:9], off
	v_mul_u32_u24_e32 v2, 0x50, v15
	v_lshlrev_b32_e32 v3, 4, v16
	v_lshl_or_b32 v10, v21, 16, v12
	v_lshl_or_b32 v12, v29, 16, v20
	v_lshl_or_b32 v13, v5, 16, v22
	v_add3_u32 v2, 0, v2, v3
	v_cmp_gt_u32_e32 vcc, s80, v14
	global_store_dwordx4 v[18:19], v[10:13], off
	ds_write_b128 v2, v[6:9] offset:19456
	s_and_saveexec_b64 s[4:5], vcc
	s_cbranch_execz .LBB0_1393
	s_lshl_b64 s[6:7], s[12:13], 9
	s_add_u32 s6, s42, s6
	v_mul_f32_e32 v4, 0x3fb8aa3b, v4
	s_addc_u32 s7, s43, s7
	v_lshlrev_b32_e32 v82, 2, v15
	v_exp_f32_e32 v4, v4
	v_lshl_add_u64 v[2:3], s[6:7], 0, v[82:83]
	v_add_co_u32_e32 v2, vcc, 0x48c82000, v2
	s_nop 1
	v_addc_co_u32_e32 v3, vcc, 0, v3, vcc
	global_store_dword v[2:3], v4, off

; __device__ __forceinline__ void hgrn_x2_unit(const Args& a, int unit) {
;     ...
;     const int vs = unit & 7, h = (unit >> 3) & 7, b = unit >> 6;
;     const bf16* QT = (const bf16*)(ws + WS_HQT); float* OI = (float*)(ws + WS_HOI);
;     const int fr = lane & 15, fg = lane >> 4;
;     f32x4 S[8];
; #pragma unroll
;     for (int i = 0; i < 8; ++i) S[i] = (f32x4){0.f, 0.f, 0.f, 0.f};
; #pragma unroll 1
;     for (int blk = 0; blk < SEQ / HB; ++blk) {
;         const int u = (b * 8 + h) * 64 + blk; const size_t tok0 = (size_t)b * SEQ + blk * HB;
;         const bf16* KT = (const bf16*)(ws + WS_HKT) + (size_t)u * 4096; const bf16* VT = (const bf16*)(ws + WS_HVT) + (size_t)u * 4096; const float* DEC = (const float*)(ws + WS_HDEC) + (size_t)u * 128;
;         FragU Aq[2][4]; f32x4 o[2]; FragU Ak[8]; f32x4 dc[8]; FragU Bv;
; #pragma unroll
;         for (int mt = 0; mt < 2; ++mt) { const bf16* qr = QT + (tok0 + 16 * mt + fr) * 1024 + h * 128;
; #pragma unroll
;             for (int ks = 0; ks < 4; ++ks) { Aq[mt][ks].h[0] = *(const u32x2*)(qr + 32 * ks + 4 * fg); Aq[mt][ks].h[1] = *(const u32x2*)(qr + 32 * ks + 16 + 4 * fg); }
; #pragma unroll
;             for (int r = 0; r < 4; ++r) o[mt][r] = OI[(tok0 + 16 * mt + 4 * fg + r) * 1024 + h * 128 + 16 * vs + fr]; }
; #pragma unroll
;         for (int dt = 0; dt < 8; ++dt) { Ak[dt].u = *(const u32x4*)(KT + (16 * dt + fr) * 32 + 8 * fg); dc[dt] = *(const f32x4*)(DEC + 16 * dt + 4 * fg); }
;         Bv.u = *(const u32x4*)(VT + (16 * vs + fr) * 32 + 8 * fg);
; template <int LAYER>
; __device__ __forceinline__ void layer_phases(const Args& args, LAS unsigned char* lds, const XcdBarrier& bar, int lo, int hi) {
;     ...
;         { int tw = threadIdx.x; asm volatile("" : "+v"(tw)); const int wv = __builtin_amdgcn_readfirstlane(tw >> 6);
;           if (G < 256) { if (wv < 2) for (int u2 = bid * 2 + wv; u2 < 256; u2 += G * 2) hgrn_x2_unit(args, u2); }
;           else if (bid < 128 && wv < 2) hgrn_x2_unit(args, bid * 2 + wv);
.LBB0_1793:
	v_mov_b32_e32 v1, v0
	s_mov_b64 s[4:5], -1
	v_readfirstlane_b32 s2, v1
	s_ashr_i32 s2, s2, 6
	s_and_b64 vcc, exec, s[14:15]
	s_cbranch_vccz .LBB0_1798
	s_cmpk_lt_i32 s60, 0x80
	s_cselect_b64 s[4:5], -1, 0
	s_cmp_lt_i32 s2, 2
	s_cselect_b64 s[6:7], -1, 0
	s_and_b64 s[4:5], s[4:5], s[6:7]
	s_andn2_b64 vcc, exec, s[4:5]
	s_cbranch_vccnz .LBB0_1797
	s_lshl_b32 s4, s60, 1
	s_add_i32 s14, s2, s4
	v_mov_b32_e32 v1, v0
	s_mov_b64 s[4:5], 0
	s_ashr_i32 s8, s14, 6
	s_load_dwordx2 s[6:7], s[0:1], 0xd0
	s_ashr_i32 s9, s8, 31
	s_waitcnt vmcnt(0)
	v_and_b32_e32 v4, 15, v1
	v_bfe_u32 v1, v1, 4, 2
	s_lshl_b64 s[10:11], s[8:9], 23
	s_bfe_u32 s15, s14, 0x30003
	v_lshl_or_b32 v2, v1, 14, s10
	s_and_b32 s14, s14, 7
	v_lshl_or_b32 v2, s15, 9, v2
	s_lshl_b32 s10, s14, 6
	v_lshlrev_b32_e32 v3, 2, v4
	s_lshl_b32 s16, s8, 9
	v_or3_b32 v2, v2, s10, v3
	v_mov_b32_e32 v3, s11
	s_lshl_b64 s[8:9], s[8:9], 22
	s_lshl_b32 s17, s15, 6
	v_lshlrev_b32_e32 v5, 3, v1
	s_waitcnt lgkmcnt(0)
	v_lshl_add_u64 v[46:47], s[6:7], 0, v[2:3]
	v_lshl_or_b32 v2, v4, 11, s8
	s_lshl_b32 s8, s15, 8
	v_or3_b32 v2, v2, s8, v5
	s_or_b32 s8, s16, s17
	v_mov_b32_e32 v3, s9
	s_ashr_i32 s9, s8, 31
	v_and_b32_e32 v250, 63, v0
	v_lshlrev_b32_e32 v250, 4, v250
	s_mul_i32 s100, s8, 0x2000
	v_add_u32_e32 v250, s100, v250
	v_mov_b32_e32 v251, 0
	v_lshl_add_u64 v[48:49], s[6:7], 0, v[250:251]
	s_lshl_b64 s[10:11], s[8:9], 13
	v_lshlrev_b32_e32 v2, 4, v1
	v_or_b32_e32 v1, s10, v2
	s_lshl_b32 s10, s14, 10
	v_lshlrev_b32_e32 v8, 6, v4
	v_or3_b32 v4, s10, v8, v1
	v_mov_b32_e32 v5, s11
	v_lshl_add_u64 v[6:7], s[6:7], 0, v[4:5]
	v_or_b32_e32 v4, v1, v8
	s_lshl_b64 s[8:9], s[8:9], 9
	v_lshl_add_u64 v[52:53], s[6:7], 0, v[4:5]
	s_add_u32 s6, s6, s8
	v_mov_b32_e32 v3, 0
	s_addc_u32 s7, s7, s9
	s_mov_b64 s[10:11], 0x47c82000
	v_lshl_add_u64 v[4:5], s[6:7], 0, v[2:3]
	s_mov_b64 s[6:7], 0x48c82100
	v_lshl_add_u64 v[50:51], v[6:7], 0, s[10:11]
	v_lshl_add_u64 v[54:55], v[4:5], 0, s[6:7]
	s_mov_b32 s16, 64
	s_mov_b32 s17, 0x45c82000
	s_mov_b32 s18, 0x48d83000
	s_mov_b32 s19, 0x48d85000
	s_mov_b32 s20, 0x45c83000
	s_mov_b32 s21, 0x48d93000
	s_mov_b32 s22, 0x48d95000
	s_mov_b32 s23, 0x46c82000
	s_mov_b32 s24, 0x46c83000
	s_mov_b64 s[6:7], 0x20000
	s_mov_b64 s[8:9], 0x2000
	s_mov_b64 s[10:11], 0x2000
	s_mov_b64 s[14:15], 0x200
	v_mov_b32_e32 v2, v3
	v_mov_b32_e32 v4, v3
	v_mov_b32_e32 v5, v3
	v_mov_b32_e32 v6, v3
	v_mov_b32_e32 v7, v3
	v_mov_b32_e32 v8, v3
	v_mov_b32_e32 v9, v3
	v_mov_b32_e32 v10, v3
	v_mov_b32_e32 v11, v3
	v_mov_b32_e32 v12, v3
	v_mov_b32_e32 v13, v3
	v_mov_b32_e32 v14, v3
	v_mov_b32_e32 v15, v3
	v_mov_b32_e32 v16, v3
	v_mov_b32_e32 v17, v3
	v_mov_b32_e32 v18, v3
	v_mov_b32_e32 v19, v3
	v_mov_b32_e32 v20, v3
	v_mov_b32_e32 v21, v3
	v_mov_b32_e32 v22, v3
	v_mov_b32_e32 v23, v3
	v_mov_b32_e32 v24, v3
	v_mov_b32_e32 v25, v3
	v_mov_b32_e32 v26, v3
	v_mov_b32_e32 v27, v3
	v_mov_b32_e32 v28, v3
	v_mov_b32_e32 v29, v3
	v_mov_b32_e32 v30, v3
	v_mov_b32_e32 v31, v3
	v_mov_b32_e32 v32, v3
	v_mov_b32_e32 v33, v3
; __device__ __forceinline__ unsigned pk2(float lo, float hi) { unsigned r; asm volatile("v_cvt_pk_bf16_f32 %0, %1, %2" : "=v"(r) : "v"(lo), "v"(hi)); return r; }
; __device__ __forceinline__ f32x4 mfma16(bf16x8 a, bf16x8 b, f32x4 c) { return __builtin_amdgcn_mfma_f32_16x16x32_bf16(a, b, c, 0, 0, 0); }
; __device__ __forceinline__ void hgrn_x2_unit(const Args& a, int unit) {
;     ...
;     for (int blk = 0; blk < SEQ / HB; ++blk) {
;         const int u = (b * 8 + h) * 64 + blk; const size_t tok0 = (size_t)b * SEQ + blk * HB;
;         const bf16* KT = (const bf16*)(ws + WS_HKT) + (size_t)u * 4096; const bf16* VT = (const bf16*)(ws + WS_HVT) + (size_t)u * 4096; const float* DEC = (const float*)(ws + WS_HDEC) + (size_t)u * 128;
;         FragU Aq[2][4]; f32x4 o[2]; FragU Ak[8]; f32x4 dc[8]; FragU Bv;
; #pragma unroll
;         for (int mt = 0; mt < 2; ++mt) { const bf16* qr = QT + (tok0 + 16 * mt + fr) * 1024 + h * 128;
; #pragma unroll
;             for (int ks = 0; ks < 4; ++ks) { Aq[mt][ks].h[0] = *(const u32x2*)(qr + 32 * ks + 4 * fg); Aq[mt][ks].h[1] = *(const u32x2*)(qr + 32 * ks + 16 + 4 * fg); }
; #pragma unroll
;             for (int r = 0; r < 4; ++r) o[mt][r] = OI[(tok0 + 16 * mt + 4 * fg + r) * 1024 + h * 128 + 16 * vs + fr]; }
; #pragma unroll
;         for (int dt = 0; dt < 8; ++dt) { Ak[dt].u = *(const u32x4*)(KT + (16 * dt + fr) * 32 + 8 * fg); dc[dt] = *(const f32x4*)(DEC + 16 * dt + 4 * fg); }
;         Bv.u = *(const u32x4*)(VT + (16 * vs + fr) * 32 + 8 * fg);
; #pragma unroll
;         for (int ks = 0; ks < 4; ++ks) { FragU Sb; Sb.u.x = pk2(S[2 * ks][0], S[2 * ks][1]); Sb.u.y = pk2(S[2 * ks][2], S[2 * ks][3]); Sb.u.z = pk2(S[2 * ks + 1][0], S[2 * ks + 1][1]); Sb.u.w = pk2(S[2 * ks + 1][2], S[2 * ks + 1][3]);
;             o[0] = mfma16(Aq[0][ks].v, Sb.v, o[0]); o[1] = mfma16(Aq[1][ks].v, Sb.v, o[1]); }
; #pragma unroll
;         for (int mt = 0; mt < 2; ++mt)
; #pragma unroll
;             for (int r = 0; r < 4; ++r) OI[(tok0 + 16 * mt + 4 * fg + r) * 1024 + h * 128 + 16 * vs + fr] = o[mt][r];
; #pragma unroll
;         for (int dt = 0; dt < 8; ++dt) S[dt] = mfma16(Ak[dt].v, Bv.v, S[dt] * dc[dt]);
.LBB0_1796:
	v_lshl_add_u64 v[34:35], v[48:49], 0, s[4:5]
	v_add_co_u32_e32 v120, vcc, s17, v34
	v_lshl_add_u64 v[36:37], v[46:47], 0, s[4:5]
	s_nop 0
	v_addc_co_u32_e32 v121, vcc, 0, v35, vcc
	v_add_co_u32_e32 v56, vcc, s18, v36
	v_lshl_add_u64 v[40:41], v[52:53], 0, s[4:5]
	s_nop 0
	v_addc_co_u32_e32 v57, vcc, 0, v37, vcc
	v_add_co_u32_e32 v58, vcc, s19, v36
	v_lshl_add_u64 v[38:39], v[54:55], 0, s[4:5]
	s_nop 0
	v_addc_co_u32_e32 v59, vcc, 0, v37, vcc
	v_add_co_u32_e32 v122, vcc, s20, v34
	v_lshl_add_u64 v[156:157], v[50:51], 0, s[4:5]
	s_nop 0
	v_addc_co_u32_e32 v123, vcc, 0, v35, vcc
	v_add_co_u32_e32 v60, vcc, s21, v36
	s_add_i32 s16, s16, -1
	s_nop 0
	v_addc_co_u32_e32 v61, vcc, 0, v37, vcc
	v_add_co_u32_e32 v62, vcc, s22, v36
	v_lshl_add_u64 v[46:47], v[46:47], 0, s[6:7]
	s_nop 0
	v_addc_co_u32_e32 v63, vcc, 0, v37, vcc
	v_add_co_u32_e32 v132, vcc, s23, v40
	v_lshl_add_u64 v[48:49], v[48:49], 0, s[8:9]
	s_nop 0
	v_addc_co_u32_e32 v133, vcc, 0, v41, vcc
	v_add_co_u32_e32 v152, vcc, s24, v40
	v_lshl_add_u64 v[50:51], v[50:51], 0, s[10:11]
	s_nop 0
	v_addc_co_u32_e32 v153, vcc, 0, v41, vcc
	global_load_dwordx4 v[64:67], v[38:39], off offset:-256
	global_load_dwordx4 v[68:71], v[38:39], off offset:-192
	global_load_dwordx4 v[72:75], v[38:39], off offset:-128
	global_load_dwordx4 v[76:79], v[38:39], off offset:-64
	global_load_dwordx4 v[80:83], v[38:39], off
	global_load_dwordx4 v[84:87], v[38:39], off offset:64
	global_load_dwordx4 v[88:91], v[38:39], off offset:128
	global_load_dwordx4 v[92:95], v[38:39], off offset:192
	global_load_dwordx4 v[96:99], v[120:121], off
	s_nop 0
	global_load_dwordx4 v[100:103], v[120:121], off offset:1024
	s_nop 0
	global_load_dwordx4 v[104:107], v[120:121], off offset:2048
	s_nop 0
	global_load_dwordx4 v[34:37], v[120:121], off offset:3072
	s_nop 0
	global_load_dwordx4 v[108:111], v[122:123], off
	s_nop 0
	global_load_dwordx4 v[112:115], v[122:123], off offset:1024
	s_nop 0
	global_load_dwordx4 v[42:45], v[122:123], off offset:2048
	s_nop 0
	global_load_dwordx4 v[38:41], v[122:123], off offset:3072
	s_nop 0
	global_load_dword v116, v[56:57], off offset:-4096
	global_load_dword v117, v[56:57], off
	global_load_dword v118, v[58:59], off offset:-4096
	global_load_dword v119, v[58:59], off
	global_load_dword v120, v[60:61], off offset:-4096
	global_load_dword v121, v[60:61], off
	global_load_dword v122, v[62:63], off offset:-4096
	global_load_dword v123, v[62:63], off
	global_load_dwordx4 v[124:127], v[132:133], off offset:1024
	global_load_dwordx4 v[128:131], v[132:133], off offset:2048
	s_nop 0
	global_load_dwordx4 v[132:135], v[132:133], off offset:3072
	s_nop 0
	global_load_dwordx4 v[136:139], v[152:153], off offset:-4096
	global_load_dwordx4 v[140:143], v[152:153], off
	global_load_dwordx4 v[144:147], v[152:153], off offset:1024
	global_load_dwordx4 v[148:151], v[152:153], off offset:2048
	s_nop 0
	global_load_dwordx4 v[152:155], v[152:153], off offset:3072
	s_nop 0
	global_load_dwordx4 v[156:159], v[156:157], off
	v_cvt_pk_bf16_f32 v160, v2, v3
	v_cvt_pk_bf16_f32 v161, v4, v5
	v_cvt_pk_bf16_f32 v162, v6, v7
	v_cvt_pk_bf16_f32 v163, v8, v9
	v_cvt_pk_bf16_f32 v164, v10, v11
	v_cvt_pk_bf16_f32 v165, v12, v13
	v_cvt_pk_bf16_f32 v166, v14, v15
	v_cvt_pk_bf16_f32 v167, v16, v17
	v_lshl_add_u64 v[52:53], v[52:53], 0, s[10:11]
	v_lshl_add_u64 v[54:55], v[54:55], 0, s[14:15]
	s_cmp_lg_u32 s16, 0
	s_waitcnt vmcnt(13)
	v_mfma_f32_16x16x32_bf16 v[96:99], v[96:99], v[160:163], v[116:119]
	v_mul_f32_e64 v6, v6, v68
	v_mul_f32_e64 v7, v7, v69
	v_pk_mul_f32 v[8:9], v[8:9], v[70:71]
	v_cvt_pk_bf16_f32 v116, v18, v19
	s_waitcnt vmcnt(9)
	v_mfma_f32_16x16x32_bf16 v[108:111], v[108:111], v[160:163], v[120:123]
	v_cvt_pk_bf16_f32 v117, v20, v21
	v_cvt_pk_bf16_f32 v118, v22, v23
	v_mul_f32_e64 v10, v10, v72
	v_mul_f32_e64 v11, v11, v73
	v_mfma_f32_16x16x32_bf16 v[68:71], v[100:103], v[164:167], v[96:99]
	v_mul_f32_e64 v12, v12, v74
	v_mul_f32_e64 v13, v13, v75
	v_cvt_pk_bf16_f32 v119, v24, v25
	v_pk_mul_f32 v[2:3], v[2:3], v[64:65]
	v_mfma_f32_16x16x32_bf16 v[72:75], v[112:115], v[164:167], v[108:111]
	v_mul_f32_e64 v4, v4, v66
	v_mul_f32_e64 v5, v5, v67
	v_pk_mul_f32 v[14:15], v[14:15], v[76:77]
	v_pk_mul_f32 v[16:17], v[16:17], v[78:79]
	v_mfma_f32_16x16x32_bf16 v[68:71], v[104:107], v[116:119], v[68:71]
	v_cvt_pk_bf16_f32 v64, v26, v27
	v_mul_f32_e64 v18, v18, v80
	v_mul_f32_e64 v19, v19, v81
	v_pk_mul_f32 v[20:21], v[20:21], v[82:83]
	v_cvt_pk_bf16_f32 v65, v28, v29
	v_pk_mul_f32 v[22:23], v[22:23], v[84:85]
	v_pk_mul_f32 v[24:25], v[24:25], v[86:87]
	v_cvt_pk_bf16_f32 v66, v30, v31
	v_pk_mul_f32 v[26:27], v[26:27], v[88:89]
	v_pk_mul_f32 v[28:29], v[28:29], v[90:91]
	v_cvt_pk_bf16_f32 v67, v32, v33
	v_pk_mul_f32 v[30:31], v[30:31], v[92:93]
	v_pk_mul_f32 v[32:33], v[32:33], v[94:95]
	s_waitcnt vmcnt(0)
	v_mfma_f32_16x16x32_bf16 v[2:5], v[136:139], v[156:159], v[2:5]
	v_mfma_f32_16x16x32_bf16 v[6:9], v[124:127], v[156:159], v[6:9]
	v_mfma_f32_16x16x32_bf16 v[10:13], v[128:131], v[156:159], v[10:13]
	v_mfma_f32_16x16x32_bf16 v[14:17], v[132:135], v[156:159], v[14:17]
	v_mfma_f32_16x16x32_bf16 v[18:21], v[140:143], v[156:159], v[18:21]
	v_mfma_f32_16x16x32_bf16 v[22:25], v[144:147], v[156:159], v[22:25]
	v_mfma_f32_16x16x32_bf16 v[26:29], v[148:151], v[156:159], v[26:29]
	v_mfma_f32_16x16x32_bf16 v[30:33], v[152:155], v[156:159], v[30:33]
	v_mfma_f32_16x16x32_bf16 v[42:45], v[42:45], v[116:119], v[72:75]
	v_mfma_f32_16x16x32_bf16 v[34:37], v[34:37], v[64:67], v[68:71]
	v_mfma_f32_16x16x32_bf16 v[38:41], v[38:41], v[64:67], v[42:45]
	s_nop 6
	global_store_dword v[56:57], v34, off offset:-4096
	global_store_dword v[56:57], v35, off
	global_store_dword v[58:59], v36, off offset:-4096
	global_store_dword v[58:59], v37, off
	global_store_dword v[60:61], v38, off offset:-4096
	global_store_dword v[60:61], v39, off
	global_store_dword v[62:63], v40, off offset:-4096
	global_store_dword v[62:63], v41, off
	s_cbranch_scc1 .LBB0_1796
